# peeled first K-tile-pair iteration of the four int8 GEMM main loops (no wave-uniform branches inside MFMA segments; pointer SALU moved behind the closing barrier)
# speedup vs baseline: 1.0035x; 1.0035x over previous
.LBB0_531:
	s_waitcnt vmcnt(8)
	s_waitcnt lgkmcnt(0)
	s_barrier
	s_setprio 1
	v_mfma_i32_16x16x64_i8 v[18:21], v[158:161], v[190:193], 0
	s_nop 0
	v_mfma_i32_16x16x64_i8 v[18:21], v[154:157], v[186:189], v[18:21]
	v_mfma_i32_16x16x64_i8 v[22:25], v[150:153], v[190:193], 0
	s_nop 0
	v_mfma_i32_16x16x64_i8 v[22:25], v[142:145], v[186:189], v[22:25]
	v_mfma_i32_16x16x64_i8 v[26:29], v[146:149], v[190:193], 0
	s_nop 0
	v_mfma_i32_16x16x64_i8 v[26:29], v[138:141], v[186:189], v[26:29]
	v_mfma_i32_16x16x64_i8 v[34:37], v[134:137], v[190:193], 0
	s_nop 0
	v_mfma_i32_16x16x64_i8 v[34:37], v[130:133], v[186:189], v[34:37]
	v_mfma_i32_16x16x64_i8 v[50:53], v[158:161], v[182:185], 0
	s_nop 0
	v_mfma_i32_16x16x64_i8 v[50:53], v[154:157], v[178:181], v[50:53]
	v_mfma_i32_16x16x64_i8 v[62:65], v[150:153], v[182:185], 0
	s_nop 0
	v_mfma_i32_16x16x64_i8 v[62:65], v[142:145], v[178:181], v[62:65]
	v_mfma_i32_16x16x64_i8 v[54:57], v[146:149], v[182:185], 0
	s_nop 0
	v_mfma_i32_16x16x64_i8 v[54:57], v[138:141], v[178:181], v[54:57]
	v_mfma_i32_16x16x64_i8 v[66:69], v[134:137], v[182:185], 0
	s_nop 0
	v_mfma_i32_16x16x64_i8 v[66:69], v[130:133], v[178:181], v[66:69]
	v_mfma_i32_16x16x64_i8 v[82:85], v[158:161], v[174:177], 0
	s_nop 0
	v_mfma_i32_16x16x64_i8 v[82:85], v[154:157], v[170:173], v[82:85]
	v_mfma_i32_16x16x64_i8 v[94:97], v[150:153], v[174:177], 0
	s_nop 0
	v_mfma_i32_16x16x64_i8 v[94:97], v[142:145], v[170:173], v[94:97]
	v_mfma_i32_16x16x64_i8 v[86:89], v[146:149], v[174:177], 0
	s_nop 0
	v_mfma_i32_16x16x64_i8 v[86:89], v[138:141], v[170:173], v[86:89]
	v_mfma_i32_16x16x64_i8 v[98:101], v[134:137], v[174:177], 0
	s_nop 0
	v_mfma_i32_16x16x64_i8 v[98:101], v[130:133], v[170:173], v[98:101]
	v_mfma_i32_16x16x64_i8 v[114:117], v[158:161], v[166:169], 0
	s_nop 0
	v_mfma_i32_16x16x64_i8 v[114:117], v[154:157], v[162:165], v[114:117]
	v_mfma_i32_16x16x64_i8 v[122:125], v[150:153], v[166:169], 0
	s_nop 0
	v_mfma_i32_16x16x64_i8 v[122:125], v[142:145], v[162:165], v[122:125]
	v_mfma_i32_16x16x64_i8 v[118:121], v[146:149], v[166:169], 0
	s_nop 0
	v_mfma_i32_16x16x64_i8 v[118:121], v[138:141], v[162:165], v[118:121]
	v_mfma_i32_16x16x64_i8 v[126:129], v[134:137], v[166:169], 0
	s_nop 0
	v_mfma_i32_16x16x64_i8 v[126:129], v[130:133], v[162:165], v[126:129]
	s_setprio 0
	s_barrier
	s_add_u32 s63, s35, s66
	s_addc_u32 s69, s60, s67
	s_cmp_eq_u32 s49, 12
	s_cselect_b64 s[82:83], -1, 0
	s_and_b64 s[70:71], s[82:83], exec
	s_cselect_b32 s79, s79, s69
	s_cselect_b32 s78, s78, s63
	s_mov_b64 s[70:71], s[78:79]
	v_mov_b32_e32 v205, v197
	s_mov_b32 m0, s19
	s_waitcnt lgkmcnt(0)
	ds_read_b128 v[190:193], v204 offset:16384
	ds_read_b128 v[186:189], v204 offset:17408
	ds_read_b128 v[182:185], v204 offset:18432
	ds_read_b128 v[178:181], v204 offset:19456
	ds_read_b128 v[174:177], v204 offset:20480
	ds_read_b128 v[170:173], v204 offset:21504
	ds_read_b128 v[166:169], v204 offset:22528
	ds_read_b128 v[162:165], v204 offset:23552
	s_nop 0
	global_load_lds_dwordx4 v205, s[70:71]
	v_mov_b32_e32 v205, v199
	s_mov_b32 m0, s20
	s_nop 0
	global_load_lds_dwordx4 v205, s[70:71]
	s_add_u32 s70, s78, 0x40000
	s_addc_u32 s71, s79, 0
	v_mov_b32_e32 v205, v197
	s_mov_b32 m0, s21
	s_nop 0
	global_load_lds_dwordx4 v205, s[70:71]
	v_mov_b32_e32 v205, v199
	s_mov_b32 m0, s22
	s_nop 0
	global_load_lds_dwordx4 v205, s[70:71]
	s_waitcnt vmcnt(6)
	s_waitcnt lgkmcnt(0)
	s_barrier
	s_setprio 1
	v_mfma_i32_16x16x64_i8 v[2:5], v[158:161], v[190:193], 0
	s_nop 0
	v_mfma_i32_16x16x64_i8 v[2:5], v[154:157], v[186:189], v[2:5]
	v_mfma_i32_16x16x64_i8 v[6:9], v[150:153], v[190:193], 0
	s_nop 0
	v_mfma_i32_16x16x64_i8 v[6:9], v[142:145], v[186:189], v[6:9]
	v_mfma_i32_16x16x64_i8 v[10:13], v[146:149], v[190:193], 0
	s_nop 0
	v_mfma_i32_16x16x64_i8 v[10:13], v[138:141], v[186:189], v[10:13]
	v_mfma_i32_16x16x64_i8 v[14:17], v[134:137], v[190:193], 0
	s_nop 0
	v_mfma_i32_16x16x64_i8 v[14:17], v[130:133], v[186:189], v[14:17]
	v_mfma_i32_16x16x64_i8 v[30:33], v[158:161], v[182:185], 0
	s_nop 0
	v_mfma_i32_16x16x64_i8 v[30:33], v[154:157], v[178:181], v[30:33]
	v_mfma_i32_16x16x64_i8 v[42:45], v[150:153], v[182:185], 0
	s_nop 0
	v_mfma_i32_16x16x64_i8 v[42:45], v[142:145], v[178:181], v[42:45]
	v_mfma_i32_16x16x64_i8 v[38:41], v[146:149], v[182:185], 0
	s_nop 0
	v_mfma_i32_16x16x64_i8 v[38:41], v[138:141], v[178:181], v[38:41]
	v_mfma_i32_16x16x64_i8 v[46:49], v[134:137], v[182:185], 0
	s_nop 0
	v_mfma_i32_16x16x64_i8 v[46:49], v[130:133], v[178:181], v[46:49]
	v_mfma_i32_16x16x64_i8 v[58:61], v[158:161], v[174:177], 0
	s_nop 0
	v_mfma_i32_16x16x64_i8 v[58:61], v[154:157], v[170:173], v[58:61]
	v_mfma_i32_16x16x64_i8 v[74:77], v[150:153], v[174:177], 0
	s_nop 0
	v_mfma_i32_16x16x64_i8 v[74:77], v[142:145], v[170:173], v[74:77]
	v_mfma_i32_16x16x64_i8 v[70:73], v[146:149], v[174:177], 0
	s_nop 0
	v_mfma_i32_16x16x64_i8 v[70:73], v[138:141], v[170:173], v[70:73]
	v_mfma_i32_16x16x64_i8 v[78:81], v[134:137], v[174:177], 0
	s_nop 0
	v_mfma_i32_16x16x64_i8 v[78:81], v[130:133], v[170:173], v[78:81]
	v_mfma_i32_16x16x64_i8 v[90:93], v[158:161], v[166:169], 0
	s_nop 0
	v_mfma_i32_16x16x64_i8 v[90:93], v[154:157], v[162:165], v[90:93]
	v_mfma_i32_16x16x64_i8 v[106:109], v[150:153], v[166:169], 0
	s_nop 0
	v_mfma_i32_16x16x64_i8 v[106:109], v[142:145], v[162:165], v[106:109]
	v_mfma_i32_16x16x64_i8 v[102:105], v[146:149], v[166:169], 0
	s_nop 0
	v_mfma_i32_16x16x64_i8 v[102:105], v[138:141], v[162:165], v[102:105]
	v_mfma_i32_16x16x64_i8 v[110:113], v[134:137], v[166:169], 0
	s_nop 0
	v_mfma_i32_16x16x64_i8 v[110:113], v[130:133], v[162:165], v[110:113]
	s_setprio 0
	s_barrier
	s_add_u32 s51, s51, 0x100
	s_addc_u32 s69, s62, 0
	s_and_b64 s[62:63], s[82:83], exec
	s_cselect_b32 s63, s77, s69
	s_cselect_b32 s62, s76, s51
	s_add_u32 s76, s78, 0x80
	s_addc_u32 s77, s79, 0
	s_add_i32 s51, 0, 0x18000
	s_add_i32 s69, 0, 0x1c000
	v_add_u32_e32 v130, s51, v202
	v_add_u32_e32 v131, s69, v202
	ds_read_b128 v[158:161], v130
	ds_read_b128 v[154:157], v130 offset:1024
	ds_read_b128 v[150:153], v130 offset:2048
	ds_read_b128 v[146:149], v130 offset:3072
	ds_read_b128 v[142:145], v131
	ds_read_b128 v[138:141], v131 offset:1024
	ds_read_b128 v[134:137], v131 offset:2048
	ds_read_b128 v[130:133], v131 offset:3072
	s_mov_b64 s[70:71], s[62:63]
	v_mov_b32_e32 v205, v196
	s_mov_b32 m0, s1
	s_waitcnt lgkmcnt(0)
	ds_read_b128 v[162:165], v204 offset:32768
	ds_read_b128 v[166:169], v204 offset:33792
	ds_read_b128 v[170:173], v204 offset:34816
	ds_read_b128 v[174:177], v204 offset:35840
	ds_read_b128 v[178:181], v204 offset:36864
	ds_read_b128 v[182:185], v204 offset:37888
	ds_read_b128 v[186:189], v204 offset:38912
	ds_read_b128 v[190:193], v204 offset:39936
	s_add_u32 s62, s62, 0x40000
	global_load_lds_dwordx4 v205, s[70:71]
	v_mov_b32_e32 v205, v198
	s_mov_b32 m0, s23
	s_addc_u32 s63, s63, 0
	global_load_lds_dwordx4 v205, s[70:71]
	v_mov_b32_e32 v205, v196
	s_mov_b32 m0, s26
	s_nop 0
	global_load_lds_dwordx4 v205, s[62:63]
	v_mov_b32_e32 v205, v198
	s_mov_b32 m0, s27
	s_nop 0
	global_load_lds_dwordx4 v205, s[62:63]
	s_waitcnt vmcnt(8)
	s_waitcnt lgkmcnt(0)
	s_barrier
	s_setprio 1
	s_waitcnt lgkmcnt(0)
	v_mfma_i32_16x16x64_i8 v[18:21], v[158:161], v[162:165], v[18:21]
	s_nop 0
	v_mfma_i32_16x16x64_i8 v[18:21], v[154:157], v[166:169], v[18:21]
	v_mfma_i32_16x16x64_i8 v[22:25], v[150:153], v[162:165], v[22:25]
	s_nop 0
	v_mfma_i32_16x16x64_i8 v[22:25], v[146:149], v[166:169], v[22:25]
	v_mfma_i32_16x16x64_i8 v[26:29], v[142:145], v[162:165], v[26:29]
	s_nop 0
	v_mfma_i32_16x16x64_i8 v[26:29], v[138:141], v[166:169], v[26:29]
	v_mfma_i32_16x16x64_i8 v[34:37], v[134:137], v[162:165], v[34:37]
	s_nop 0
	v_mfma_i32_16x16x64_i8 v[34:37], v[130:133], v[166:169], v[34:37]
	v_mfma_i32_16x16x64_i8 v[50:53], v[158:161], v[170:173], v[50:53]
	s_nop 0
	v_mfma_i32_16x16x64_i8 v[50:53], v[154:157], v[174:177], v[50:53]
	v_mfma_i32_16x16x64_i8 v[62:65], v[150:153], v[170:173], v[62:65]
	s_nop 0
	v_mfma_i32_16x16x64_i8 v[62:65], v[146:149], v[174:177], v[62:65]
	v_mfma_i32_16x16x64_i8 v[54:57], v[142:145], v[170:173], v[54:57]
	s_nop 0
	v_mfma_i32_16x16x64_i8 v[54:57], v[138:141], v[174:177], v[54:57]
	v_mfma_i32_16x16x64_i8 v[66:69], v[134:137], v[170:173], v[66:69]
	s_nop 0
	v_mfma_i32_16x16x64_i8 v[66:69], v[130:133], v[174:177], v[66:69]
	v_mfma_i32_16x16x64_i8 v[82:85], v[158:161], v[178:181], v[82:85]
	s_nop 0
	v_mfma_i32_16x16x64_i8 v[82:85], v[154:157], v[182:185], v[82:85]
	v_mfma_i32_16x16x64_i8 v[94:97], v[150:153], v[178:181], v[94:97]
	s_nop 0
	v_mfma_i32_16x16x64_i8 v[94:97], v[146:149], v[182:185], v[94:97]
	v_mfma_i32_16x16x64_i8 v[86:89], v[142:145], v[178:181], v[86:89]
	s_nop 0
	v_mfma_i32_16x16x64_i8 v[86:89], v[138:141], v[182:185], v[86:89]
	v_mfma_i32_16x16x64_i8 v[98:101], v[134:137], v[178:181], v[98:101]
	s_nop 0
	v_mfma_i32_16x16x64_i8 v[98:101], v[130:133], v[182:185], v[98:101]
	v_mfma_i32_16x16x64_i8 v[114:117], v[158:161], v[186:189], v[114:117]
	s_nop 0
	v_mfma_i32_16x16x64_i8 v[114:117], v[154:157], v[190:193], v[114:117]
	v_mfma_i32_16x16x64_i8 v[122:125], v[150:153], v[186:189], v[122:125]
	s_nop 0
	v_mfma_i32_16x16x64_i8 v[122:125], v[146:149], v[190:193], v[122:125]
	v_mfma_i32_16x16x64_i8 v[118:121], v[142:145], v[186:189], v[118:121]
	s_nop 0
	v_mfma_i32_16x16x64_i8 v[118:121], v[138:141], v[190:193], v[118:121]
	v_mfma_i32_16x16x64_i8 v[126:129], v[134:137], v[186:189], v[126:129]
	s_nop 0
	v_mfma_i32_16x16x64_i8 v[126:129], v[130:133], v[190:193], v[126:129]
	s_setprio 0
	s_barrier
	v_mov_b32_e32 v205, v197
	s_add_i32 s51, s51, s10
	ds_read_b128 v[162:165], v204 offset:49152
	ds_read_b128 v[166:169], v204 offset:50176
	ds_read_b128 v[170:173], v204 offset:51200
	ds_read_b128 v[174:177], v204 offset:52224
	ds_read_b128 v[178:181], v204 offset:53248
	ds_read_b128 v[182:185], v204 offset:54272
	ds_read_b128 v[186:189], v204 offset:55296
	ds_read_b128 v[190:193], v204 offset:56320
	s_mov_b32 m0, s51
	s_nop 0
	global_load_lds_dwordx4 v205, s[76:77]
	v_mov_b32_e32 v205, v199
	s_add_i32 m0, s51, 0x2000
	s_add_u32 s62, s78, 0x40080
	global_load_lds_dwordx4 v205, s[76:77]
	s_addc_u32 s63, s79, 0
	v_mov_b32_e32 v205, v197
	s_add_i32 s51, s69, s10
	s_mov_b32 m0, s51
	s_nop 0
	global_load_lds_dwordx4 v205, s[62:63]
	v_mov_b32_e32 v205, v199
	s_add_i32 m0, s51, 0x2000
	s_nop 0
	global_load_lds_dwordx4 v205, s[62:63]
	s_waitcnt vmcnt(6)
	s_waitcnt lgkmcnt(0)
	s_barrier
	s_setprio 1
	s_waitcnt lgkmcnt(0)
	v_mfma_i32_16x16x64_i8 v[2:5], v[158:161], v[162:165], v[2:5]
	s_nop 0
	v_mfma_i32_16x16x64_i8 v[2:5], v[154:157], v[166:169], v[2:5]
	v_mfma_i32_16x16x64_i8 v[6:9], v[150:153], v[162:165], v[6:9]
	s_nop 0
	v_mfma_i32_16x16x64_i8 v[6:9], v[146:149], v[166:169], v[6:9]
	v_mfma_i32_16x16x64_i8 v[10:13], v[142:145], v[162:165], v[10:13]
	s_nop 0
	v_mfma_i32_16x16x64_i8 v[10:13], v[138:141], v[166:169], v[10:13]
	v_mfma_i32_16x16x64_i8 v[14:17], v[134:137], v[162:165], v[14:17]
	s_nop 0
	v_mfma_i32_16x16x64_i8 v[14:17], v[130:133], v[166:169], v[14:17]
	v_mfma_i32_16x16x64_i8 v[30:33], v[158:161], v[170:173], v[30:33]
	s_nop 0
	v_mfma_i32_16x16x64_i8 v[30:33], v[154:157], v[174:177], v[30:33]
	v_mfma_i32_16x16x64_i8 v[42:45], v[150:153], v[170:173], v[42:45]
	s_nop 0
	v_mfma_i32_16x16x64_i8 v[42:45], v[146:149], v[174:177], v[42:45]
	v_mfma_i32_16x16x64_i8 v[38:41], v[142:145], v[170:173], v[38:41]
	s_nop 0
	v_mfma_i32_16x16x64_i8 v[38:41], v[138:141], v[174:177], v[38:41]
	v_mfma_i32_16x16x64_i8 v[46:49], v[134:137], v[170:173], v[46:49]
	s_nop 0
	v_mfma_i32_16x16x64_i8 v[46:49], v[130:133], v[174:177], v[46:49]
	v_mfma_i32_16x16x64_i8 v[58:61], v[158:161], v[178:181], v[58:61]
	s_nop 0
	v_mfma_i32_16x16x64_i8 v[58:61], v[154:157], v[182:185], v[58:61]
	v_mfma_i32_16x16x64_i8 v[74:77], v[150:153], v[178:181], v[74:77]
	s_nop 0
	v_mfma_i32_16x16x64_i8 v[74:77], v[146:149], v[182:185], v[74:77]
	v_mfma_i32_16x16x64_i8 v[70:73], v[142:145], v[178:181], v[70:73]
	s_nop 0
	v_mfma_i32_16x16x64_i8 v[70:73], v[138:141], v[182:185], v[70:73]
	v_mfma_i32_16x16x64_i8 v[78:81], v[134:137], v[178:181], v[78:81]
	s_nop 0
	v_mfma_i32_16x16x64_i8 v[78:81], v[130:133], v[182:185], v[78:81]
	v_mfma_i32_16x16x64_i8 v[90:93], v[158:161], v[186:189], v[90:93]
	s_nop 0
	v_mfma_i32_16x16x64_i8 v[90:93], v[154:157], v[190:193], v[90:93]
	v_mfma_i32_16x16x64_i8 v[106:109], v[150:153], v[186:189], v[106:109]
	s_nop 0
	v_mfma_i32_16x16x64_i8 v[106:109], v[146:149], v[190:193], v[106:109]
	v_mfma_i32_16x16x64_i8 v[102:105], v[142:145], v[186:189], v[102:105]
	s_nop 0
	v_mfma_i32_16x16x64_i8 v[102:105], v[138:141], v[190:193], v[102:105]
	v_mfma_i32_16x16x64_i8 v[110:113], v[134:137], v[186:189], v[110:113]
	s_nop 0
	v_mfma_i32_16x16x64_i8 v[110:113], v[130:133], v[190:193], v[110:113]
	s_setprio 0
	s_barrier
	s_add_i32 s49, s49, 2
	s_add_u32 s66, s66, 0x100
	s_addc_u32 s67, s67, 0
	s_cmp_gt_u32 s49, 13
	s_cbranch_scc1 .LBB0_541
	s_mov_b64 s[78:79], s[8:9]
	s_mov_b64 s[76:77], s[40:41]

.Li8b_531_527:
	s_waitcnt vmcnt(8)
	s_waitcnt lgkmcnt(0)
	s_barrier
	s_setprio 1
	v_mfma_i32_16x16x64_i8 v[18:21], v[158:161], v[190:193], v[18:21]
	s_nop 0
	v_mfma_i32_16x16x64_i8 v[18:21], v[154:157], v[186:189], v[18:21]
	v_mfma_i32_16x16x64_i8 v[22:25], v[150:153], v[190:193], v[22:25]
	s_nop 0
	v_mfma_i32_16x16x64_i8 v[22:25], v[142:145], v[186:189], v[22:25]
	v_mfma_i32_16x16x64_i8 v[26:29], v[146:149], v[190:193], v[26:29]
	s_nop 0
	v_mfma_i32_16x16x64_i8 v[26:29], v[138:141], v[186:189], v[26:29]
	v_mfma_i32_16x16x64_i8 v[34:37], v[134:137], v[190:193], v[34:37]
	s_nop 0
	v_mfma_i32_16x16x64_i8 v[34:37], v[130:133], v[186:189], v[34:37]
	v_mfma_i32_16x16x64_i8 v[50:53], v[158:161], v[182:185], v[50:53]
	s_nop 0
	v_mfma_i32_16x16x64_i8 v[50:53], v[154:157], v[178:181], v[50:53]
	v_mfma_i32_16x16x64_i8 v[62:65], v[150:153], v[182:185], v[62:65]
	s_nop 0
	v_mfma_i32_16x16x64_i8 v[62:65], v[142:145], v[178:181], v[62:65]
	v_mfma_i32_16x16x64_i8 v[54:57], v[146:149], v[182:185], v[54:57]
	s_nop 0
	v_mfma_i32_16x16x64_i8 v[54:57], v[138:141], v[178:181], v[54:57]
	v_mfma_i32_16x16x64_i8 v[66:69], v[134:137], v[182:185], v[66:69]
	s_nop 0
	v_mfma_i32_16x16x64_i8 v[66:69], v[130:133], v[178:181], v[66:69]
	v_mfma_i32_16x16x64_i8 v[82:85], v[158:161], v[174:177], v[82:85]
	s_nop 0
	v_mfma_i32_16x16x64_i8 v[82:85], v[154:157], v[170:173], v[82:85]
	v_mfma_i32_16x16x64_i8 v[94:97], v[150:153], v[174:177], v[94:97]
	s_nop 0
	v_mfma_i32_16x16x64_i8 v[94:97], v[142:145], v[170:173], v[94:97]
	v_mfma_i32_16x16x64_i8 v[86:89], v[146:149], v[174:177], v[86:89]
	s_nop 0
	v_mfma_i32_16x16x64_i8 v[86:89], v[138:141], v[170:173], v[86:89]
	v_mfma_i32_16x16x64_i8 v[98:101], v[134:137], v[174:177], v[98:101]
	s_nop 0
	v_mfma_i32_16x16x64_i8 v[98:101], v[130:133], v[170:173], v[98:101]
	v_mfma_i32_16x16x64_i8 v[114:117], v[158:161], v[166:169], v[114:117]
	s_nop 0
	v_mfma_i32_16x16x64_i8 v[114:117], v[154:157], v[162:165], v[114:117]
	v_mfma_i32_16x16x64_i8 v[122:125], v[150:153], v[166:169], v[122:125]
	s_nop 0
	v_mfma_i32_16x16x64_i8 v[122:125], v[142:145], v[162:165], v[122:125]
	v_mfma_i32_16x16x64_i8 v[118:121], v[146:149], v[166:169], v[118:121]
	s_nop 0
	v_mfma_i32_16x16x64_i8 v[118:121], v[138:141], v[162:165], v[118:121]
	v_mfma_i32_16x16x64_i8 v[126:129], v[134:137], v[166:169], v[126:129]
	s_nop 0
	v_mfma_i32_16x16x64_i8 v[126:129], v[130:133], v[162:165], v[126:129]
	s_setprio 0
	s_barrier
	s_add_u32 s63, s35, s66
	s_addc_u32 s69, s60, s67
	s_cmp_eq_u32 s49, 12
	s_cselect_b64 s[82:83], -1, 0
	s_and_b64 s[70:71], s[82:83], exec
	s_cselect_b32 s79, s79, s69
	s_cselect_b32 s78, s78, s63
	s_mov_b64 s[70:71], s[78:79]
	v_mov_b32_e32 v205, v197
	s_mov_b32 m0, s19
	s_waitcnt lgkmcnt(0)
	ds_read_b128 v[190:193], v204 offset:16384
	ds_read_b128 v[186:189], v204 offset:17408
	ds_read_b128 v[182:185], v204 offset:18432
	ds_read_b128 v[178:181], v204 offset:19456
	ds_read_b128 v[174:177], v204 offset:20480
	ds_read_b128 v[170:173], v204 offset:21504
	ds_read_b128 v[166:169], v204 offset:22528
	ds_read_b128 v[162:165], v204 offset:23552
	s_nop 0
	global_load_lds_dwordx4 v205, s[70:71]
	v_mov_b32_e32 v205, v199
	s_mov_b32 m0, s20
	s_nop 0
	global_load_lds_dwordx4 v205, s[70:71]
	s_add_u32 s70, s78, 0x40000
	s_addc_u32 s71, s79, 0
	v_mov_b32_e32 v205, v197
	s_mov_b32 m0, s21
	s_nop 0
	global_load_lds_dwordx4 v205, s[70:71]
	v_mov_b32_e32 v205, v199
	s_mov_b32 m0, s22
	s_nop 0
	global_load_lds_dwordx4 v205, s[70:71]
	s_waitcnt vmcnt(6)
	s_waitcnt lgkmcnt(0)
	s_barrier
	s_setprio 1
	v_mfma_i32_16x16x64_i8 v[2:5], v[158:161], v[190:193], v[2:5]
	s_nop 0
	v_mfma_i32_16x16x64_i8 v[2:5], v[154:157], v[186:189], v[2:5]
	v_mfma_i32_16x16x64_i8 v[6:9], v[150:153], v[190:193], v[6:9]
	s_nop 0
	v_mfma_i32_16x16x64_i8 v[6:9], v[142:145], v[186:189], v[6:9]
	v_mfma_i32_16x16x64_i8 v[10:13], v[146:149], v[190:193], v[10:13]
	s_nop 0
	v_mfma_i32_16x16x64_i8 v[10:13], v[138:141], v[186:189], v[10:13]
	v_mfma_i32_16x16x64_i8 v[14:17], v[134:137], v[190:193], v[14:17]
	s_nop 0
	v_mfma_i32_16x16x64_i8 v[14:17], v[130:133], v[186:189], v[14:17]
	v_mfma_i32_16x16x64_i8 v[30:33], v[158:161], v[182:185], v[30:33]
	s_nop 0
	v_mfma_i32_16x16x64_i8 v[30:33], v[154:157], v[178:181], v[30:33]
	v_mfma_i32_16x16x64_i8 v[42:45], v[150:153], v[182:185], v[42:45]
	s_nop 0
	v_mfma_i32_16x16x64_i8 v[42:45], v[142:145], v[178:181], v[42:45]
	v_mfma_i32_16x16x64_i8 v[38:41], v[146:149], v[182:185], v[38:41]
	s_nop 0
	v_mfma_i32_16x16x64_i8 v[38:41], v[138:141], v[178:181], v[38:41]
	v_mfma_i32_16x16x64_i8 v[46:49], v[134:137], v[182:185], v[46:49]
	s_nop 0
	v_mfma_i32_16x16x64_i8 v[46:49], v[130:133], v[178:181], v[46:49]
	v_mfma_i32_16x16x64_i8 v[58:61], v[158:161], v[174:177], v[58:61]
	s_nop 0
	v_mfma_i32_16x16x64_i8 v[58:61], v[154:157], v[170:173], v[58:61]
	v_mfma_i32_16x16x64_i8 v[74:77], v[150:153], v[174:177], v[74:77]
	s_nop 0
	v_mfma_i32_16x16x64_i8 v[74:77], v[142:145], v[170:173], v[74:77]
	v_mfma_i32_16x16x64_i8 v[70:73], v[146:149], v[174:177], v[70:73]
	s_nop 0
	v_mfma_i32_16x16x64_i8 v[70:73], v[138:141], v[170:173], v[70:73]
	v_mfma_i32_16x16x64_i8 v[78:81], v[134:137], v[174:177], v[78:81]
	s_nop 0
	v_mfma_i32_16x16x64_i8 v[78:81], v[130:133], v[170:173], v[78:81]
	v_mfma_i32_16x16x64_i8 v[90:93], v[158:161], v[166:169], v[90:93]
	s_nop 0
	v_mfma_i32_16x16x64_i8 v[90:93], v[154:157], v[162:165], v[90:93]
	v_mfma_i32_16x16x64_i8 v[106:109], v[150:153], v[166:169], v[106:109]
	s_nop 0
	v_mfma_i32_16x16x64_i8 v[106:109], v[142:145], v[162:165], v[106:109]
	v_mfma_i32_16x16x64_i8 v[102:105], v[146:149], v[166:169], v[102:105]
	s_nop 0
	v_mfma_i32_16x16x64_i8 v[102:105], v[138:141], v[162:165], v[102:105]
	v_mfma_i32_16x16x64_i8 v[110:113], v[134:137], v[166:169], v[110:113]
	s_nop 0
	v_mfma_i32_16x16x64_i8 v[110:113], v[130:133], v[162:165], v[110:113]
	s_setprio 0
	s_barrier
	s_add_u32 s51, s51, 0x100
	s_addc_u32 s69, s62, 0
	s_and_b64 s[62:63], s[82:83], exec
	s_cselect_b32 s63, s77, s69
	s_cselect_b32 s62, s76, s51
	s_add_u32 s76, s78, 0x80
	s_addc_u32 s77, s79, 0
	s_add_i32 s51, 0, 0x18000
	s_add_i32 s69, 0, 0x1c000
	v_add_u32_e32 v130, s51, v202
	v_add_u32_e32 v131, s69, v202
	ds_read_b128 v[158:161], v130
	ds_read_b128 v[154:157], v130 offset:1024
	ds_read_b128 v[150:153], v130 offset:2048
	ds_read_b128 v[146:149], v130 offset:3072
	ds_read_b128 v[142:145], v131
	ds_read_b128 v[138:141], v131 offset:1024
	ds_read_b128 v[134:137], v131 offset:2048
	ds_read_b128 v[130:133], v131 offset:3072
	s_mov_b64 s[70:71], s[62:63]
	v_mov_b32_e32 v205, v196
	s_mov_b32 m0, s1
	s_waitcnt lgkmcnt(0)
	ds_read_b128 v[162:165], v204 offset:32768
	ds_read_b128 v[166:169], v204 offset:33792
	ds_read_b128 v[170:173], v204 offset:34816
	ds_read_b128 v[174:177], v204 offset:35840
	ds_read_b128 v[178:181], v204 offset:36864
	ds_read_b128 v[182:185], v204 offset:37888
	ds_read_b128 v[186:189], v204 offset:38912
	ds_read_b128 v[190:193], v204 offset:39936
	s_add_u32 s62, s62, 0x40000
	global_load_lds_dwordx4 v205, s[70:71]
	v_mov_b32_e32 v205, v198
	s_mov_b32 m0, s23
	s_addc_u32 s63, s63, 0
	global_load_lds_dwordx4 v205, s[70:71]
	v_mov_b32_e32 v205, v196
	s_mov_b32 m0, s26
	s_nop 0
	global_load_lds_dwordx4 v205, s[62:63]
	v_mov_b32_e32 v205, v198
	s_mov_b32 m0, s27
	s_nop 0
	global_load_lds_dwordx4 v205, s[62:63]
	s_waitcnt vmcnt(8)
	s_waitcnt lgkmcnt(0)
	s_barrier
	s_setprio 1
	s_waitcnt lgkmcnt(0)
	v_mfma_i32_16x16x64_i8 v[18:21], v[158:161], v[162:165], v[18:21]
	s_nop 0
	v_mfma_i32_16x16x64_i8 v[18:21], v[154:157], v[166:169], v[18:21]
	v_mfma_i32_16x16x64_i8 v[22:25], v[150:153], v[162:165], v[22:25]
	s_nop 0
	v_mfma_i32_16x16x64_i8 v[22:25], v[146:149], v[166:169], v[22:25]
	v_mfma_i32_16x16x64_i8 v[26:29], v[142:145], v[162:165], v[26:29]
	s_nop 0
	v_mfma_i32_16x16x64_i8 v[26:29], v[138:141], v[166:169], v[26:29]
	v_mfma_i32_16x16x64_i8 v[34:37], v[134:137], v[162:165], v[34:37]
	s_nop 0
	v_mfma_i32_16x16x64_i8 v[34:37], v[130:133], v[166:169], v[34:37]
	v_mfma_i32_16x16x64_i8 v[50:53], v[158:161], v[170:173], v[50:53]
	s_nop 0
	v_mfma_i32_16x16x64_i8 v[50:53], v[154:157], v[174:177], v[50:53]
	v_mfma_i32_16x16x64_i8 v[62:65], v[150:153], v[170:173], v[62:65]
	s_nop 0
	v_mfma_i32_16x16x64_i8 v[62:65], v[146:149], v[174:177], v[62:65]
	v_mfma_i32_16x16x64_i8 v[54:57], v[142:145], v[170:173], v[54:57]
	s_nop 0
	v_mfma_i32_16x16x64_i8 v[54:57], v[138:141], v[174:177], v[54:57]
	v_mfma_i32_16x16x64_i8 v[66:69], v[134:137], v[170:173], v[66:69]
	s_nop 0
	v_mfma_i32_16x16x64_i8 v[66:69], v[130:133], v[174:177], v[66:69]
	v_mfma_i32_16x16x64_i8 v[82:85], v[158:161], v[178:181], v[82:85]
	s_nop 0
	v_mfma_i32_16x16x64_i8 v[82:85], v[154:157], v[182:185], v[82:85]
	v_mfma_i32_16x16x64_i8 v[94:97], v[150:153], v[178:181], v[94:97]
	s_nop 0
	v_mfma_i32_16x16x64_i8 v[94:97], v[146:149], v[182:185], v[94:97]
	v_mfma_i32_16x16x64_i8 v[86:89], v[142:145], v[178:181], v[86:89]
	s_nop 0
	v_mfma_i32_16x16x64_i8 v[86:89], v[138:141], v[182:185], v[86:89]
	v_mfma_i32_16x16x64_i8 v[98:101], v[134:137], v[178:181], v[98:101]
	s_nop 0
	v_mfma_i32_16x16x64_i8 v[98:101], v[130:133], v[182:185], v[98:101]
	v_mfma_i32_16x16x64_i8 v[114:117], v[158:161], v[186:189], v[114:117]
	s_nop 0
	v_mfma_i32_16x16x64_i8 v[114:117], v[154:157], v[190:193], v[114:117]
	v_mfma_i32_16x16x64_i8 v[122:125], v[150:153], v[186:189], v[122:125]
	s_nop 0
	v_mfma_i32_16x16x64_i8 v[122:125], v[146:149], v[190:193], v[122:125]
	v_mfma_i32_16x16x64_i8 v[118:121], v[142:145], v[186:189], v[118:121]
	s_nop 0
	v_mfma_i32_16x16x64_i8 v[118:121], v[138:141], v[190:193], v[118:121]
	v_mfma_i32_16x16x64_i8 v[126:129], v[134:137], v[186:189], v[126:129]
	s_nop 0
	v_mfma_i32_16x16x64_i8 v[126:129], v[130:133], v[190:193], v[126:129]
	s_setprio 0
	s_barrier
	v_mov_b32_e32 v205, v197
	s_add_i32 s51, s51, s10
	ds_read_b128 v[162:165], v204 offset:49152
	ds_read_b128 v[166:169], v204 offset:50176
	ds_read_b128 v[170:173], v204 offset:51200
	ds_read_b128 v[174:177], v204 offset:52224
	ds_read_b128 v[178:181], v204 offset:53248
	ds_read_b128 v[182:185], v204 offset:54272
	ds_read_b128 v[186:189], v204 offset:55296
	ds_read_b128 v[190:193], v204 offset:56320
	s_mov_b32 m0, s51
	s_nop 0
	global_load_lds_dwordx4 v205, s[76:77]
	v_mov_b32_e32 v205, v199
	s_add_i32 m0, s51, 0x2000
	s_add_u32 s62, s78, 0x40080
	global_load_lds_dwordx4 v205, s[76:77]
	s_addc_u32 s63, s79, 0
	v_mov_b32_e32 v205, v197
	s_add_i32 s51, s69, s10
	s_mov_b32 m0, s51
	s_nop 0
	global_load_lds_dwordx4 v205, s[62:63]
	v_mov_b32_e32 v205, v199
	s_add_i32 m0, s51, 0x2000
	s_nop 0
	global_load_lds_dwordx4 v205, s[62:63]
	s_waitcnt vmcnt(6)
	s_waitcnt lgkmcnt(0)
	s_barrier
	s_setprio 1
	s_waitcnt lgkmcnt(0)
	v_mfma_i32_16x16x64_i8 v[2:5], v[158:161], v[162:165], v[2:5]
	s_nop 0
	v_mfma_i32_16x16x64_i8 v[2:5], v[154:157], v[166:169], v[2:5]
	v_mfma_i32_16x16x64_i8 v[6:9], v[150:153], v[162:165], v[6:9]
	s_nop 0
	v_mfma_i32_16x16x64_i8 v[6:9], v[146:149], v[166:169], v[6:9]
	v_mfma_i32_16x16x64_i8 v[10:13], v[142:145], v[162:165], v[10:13]
	s_nop 0
	v_mfma_i32_16x16x64_i8 v[10:13], v[138:141], v[166:169], v[10:13]
	v_mfma_i32_16x16x64_i8 v[14:17], v[134:137], v[162:165], v[14:17]
	s_nop 0
	v_mfma_i32_16x16x64_i8 v[14:17], v[130:133], v[166:169], v[14:17]
	v_mfma_i32_16x16x64_i8 v[30:33], v[158:161], v[170:173], v[30:33]
	s_nop 0
	v_mfma_i32_16x16x64_i8 v[30:33], v[154:157], v[174:177], v[30:33]
	v_mfma_i32_16x16x64_i8 v[42:45], v[150:153], v[170:173], v[42:45]
	s_nop 0
	v_mfma_i32_16x16x64_i8 v[42:45], v[146:149], v[174:177], v[42:45]
	v_mfma_i32_16x16x64_i8 v[38:41], v[142:145], v[170:173], v[38:41]
	s_nop 0
	v_mfma_i32_16x16x64_i8 v[38:41], v[138:141], v[174:177], v[38:41]
	v_mfma_i32_16x16x64_i8 v[46:49], v[134:137], v[170:173], v[46:49]
	s_nop 0
	v_mfma_i32_16x16x64_i8 v[46:49], v[130:133], v[174:177], v[46:49]
	v_mfma_i32_16x16x64_i8 v[58:61], v[158:161], v[178:181], v[58:61]
	s_nop 0
	v_mfma_i32_16x16x64_i8 v[58:61], v[154:157], v[182:185], v[58:61]
	v_mfma_i32_16x16x64_i8 v[74:77], v[150:153], v[178:181], v[74:77]
	s_nop 0
	v_mfma_i32_16x16x64_i8 v[74:77], v[146:149], v[182:185], v[74:77]
	v_mfma_i32_16x16x64_i8 v[70:73], v[142:145], v[178:181], v[70:73]
	s_nop 0
	v_mfma_i32_16x16x64_i8 v[70:73], v[138:141], v[182:185], v[70:73]
	v_mfma_i32_16x16x64_i8 v[78:81], v[134:137], v[178:181], v[78:81]
	s_nop 0
	v_mfma_i32_16x16x64_i8 v[78:81], v[130:133], v[182:185], v[78:81]
	v_mfma_i32_16x16x64_i8 v[90:93], v[158:161], v[186:189], v[90:93]
	s_nop 0
	v_mfma_i32_16x16x64_i8 v[90:93], v[154:157], v[190:193], v[90:93]
	v_mfma_i32_16x16x64_i8 v[106:109], v[150:153], v[186:189], v[106:109]
	s_nop 0
	v_mfma_i32_16x16x64_i8 v[106:109], v[146:149], v[190:193], v[106:109]
	v_mfma_i32_16x16x64_i8 v[102:105], v[142:145], v[186:189], v[102:105]
	s_nop 0
	v_mfma_i32_16x16x64_i8 v[102:105], v[138:141], v[190:193], v[102:105]
	v_mfma_i32_16x16x64_i8 v[110:113], v[134:137], v[186:189], v[110:113]
	s_nop 0
	v_mfma_i32_16x16x64_i8 v[110:113], v[130:133], v[190:193], v[110:113]
	s_setprio 0
	s_barrier
	s_add_i32 s49, s49, 2
	s_add_u32 s66, s66, 0x100
	s_addc_u32 s67, s67, 0
	s_cmp_gt_u32 s49, 13
	s_cbranch_scc1 .LBB0_541
	s_mov_b64 s[78:79], s[8:9]
	s_mov_b64 s[76:77], s[40:41]
	s_branch .Li8loop_527

.LBB0_851:
	s_waitcnt vmcnt(8)
	s_waitcnt lgkmcnt(0)
	s_barrier
	s_setprio 1
	v_mfma_i32_16x16x64_i8 v[18:21], v[158:161], v[190:193], 0
	s_nop 0
	v_mfma_i32_16x16x64_i8 v[18:21], v[154:157], v[186:189], v[18:21]
	v_mfma_i32_16x16x64_i8 v[22:25], v[150:153], v[190:193], 0
	s_nop 0
	v_mfma_i32_16x16x64_i8 v[22:25], v[142:145], v[186:189], v[22:25]
	v_mfma_i32_16x16x64_i8 v[26:29], v[146:149], v[190:193], 0
	s_nop 0
	v_mfma_i32_16x16x64_i8 v[26:29], v[138:141], v[186:189], v[26:29]
	v_mfma_i32_16x16x64_i8 v[34:37], v[134:137], v[190:193], 0
	s_nop 0
	v_mfma_i32_16x16x64_i8 v[34:37], v[130:133], v[186:189], v[34:37]
	v_mfma_i32_16x16x64_i8 v[50:53], v[158:161], v[182:185], 0
	s_nop 0
	v_mfma_i32_16x16x64_i8 v[50:53], v[154:157], v[178:181], v[50:53]
	v_mfma_i32_16x16x64_i8 v[62:65], v[150:153], v[182:185], 0
	s_nop 0
	v_mfma_i32_16x16x64_i8 v[62:65], v[142:145], v[178:181], v[62:65]
	v_mfma_i32_16x16x64_i8 v[54:57], v[146:149], v[182:185], 0
	s_nop 0
	v_mfma_i32_16x16x64_i8 v[54:57], v[138:141], v[178:181], v[54:57]
	v_mfma_i32_16x16x64_i8 v[66:69], v[134:137], v[182:185], 0
	s_nop 0
	v_mfma_i32_16x16x64_i8 v[66:69], v[130:133], v[178:181], v[66:69]
	v_mfma_i32_16x16x64_i8 v[82:85], v[158:161], v[174:177], 0
	s_nop 0
	v_mfma_i32_16x16x64_i8 v[82:85], v[154:157], v[170:173], v[82:85]
	v_mfma_i32_16x16x64_i8 v[94:97], v[150:153], v[174:177], 0
	s_nop 0
	v_mfma_i32_16x16x64_i8 v[94:97], v[142:145], v[170:173], v[94:97]
	v_mfma_i32_16x16x64_i8 v[86:89], v[146:149], v[174:177], 0
	s_nop 0
	v_mfma_i32_16x16x64_i8 v[86:89], v[138:141], v[170:173], v[86:89]
	v_mfma_i32_16x16x64_i8 v[98:101], v[134:137], v[174:177], 0
	s_nop 0
	v_mfma_i32_16x16x64_i8 v[98:101], v[130:133], v[170:173], v[98:101]
	v_mfma_i32_16x16x64_i8 v[114:117], v[158:161], v[166:169], 0
	s_nop 0
	v_mfma_i32_16x16x64_i8 v[114:117], v[154:157], v[162:165], v[114:117]
	v_mfma_i32_16x16x64_i8 v[122:125], v[150:153], v[166:169], 0
	s_nop 0
	v_mfma_i32_16x16x64_i8 v[122:125], v[142:145], v[162:165], v[122:125]
	v_mfma_i32_16x16x64_i8 v[118:121], v[146:149], v[166:169], 0
	s_nop 0
	v_mfma_i32_16x16x64_i8 v[118:121], v[138:141], v[162:165], v[118:121]
	v_mfma_i32_16x16x64_i8 v[126:129], v[134:137], v[166:169], 0
	s_nop 0
	v_mfma_i32_16x16x64_i8 v[126:129], v[130:133], v[162:165], v[126:129]
	s_setprio 0
	s_barrier
	s_add_u32 s81, s74, s50
	s_addc_u32 s82, s75, s51
	s_cmp_eq_u32 s43, 12
	s_cselect_b64 s[76:77], -1, 0
	s_and_b64 s[78:79], s[76:77], exec
	s_cselect_b32 s65, s65, s82
	s_cselect_b32 s64, s64, s81
	s_mov_b64 s[78:79], s[64:65]
	v_mov_b32_e32 v209, v202
	s_mov_b32 m0, s21
	s_waitcnt lgkmcnt(0)
	ds_read_b128 v[190:193], v207 offset:16384
	ds_read_b128 v[186:189], v207 offset:17408
	ds_read_b128 v[182:185], v207 offset:18432
	ds_read_b128 v[178:181], v207 offset:19456
	ds_read_b128 v[174:177], v207 offset:20480
	ds_read_b128 v[170:173], v207 offset:21504
	ds_read_b128 v[166:169], v207 offset:22528
	ds_read_b128 v[162:165], v207 offset:23552
	s_nop 0
	global_load_lds_dwordx4 v209, s[78:79]
	v_mov_b32_e32 v209, v204
	s_mov_b32 m0, s33
	s_nop 0
	global_load_lds_dwordx4 v209, s[78:79]
	s_add_u32 s78, s64, 0x40000
	s_addc_u32 s79, s65, 0
	v_mov_b32_e32 v209, v202
	s_mov_b32 m0, s35
	s_nop 0
	global_load_lds_dwordx4 v209, s[78:79]
	v_mov_b32_e32 v209, v204
	s_mov_b32 m0, s60
	s_nop 0
	global_load_lds_dwordx4 v209, s[78:79]
	s_waitcnt vmcnt(6)
	s_waitcnt lgkmcnt(0)
	s_barrier
	s_setprio 1
	v_mfma_i32_16x16x64_i8 v[2:5], v[158:161], v[190:193], 0
	s_nop 0
	v_mfma_i32_16x16x64_i8 v[2:5], v[154:157], v[186:189], v[2:5]
	v_mfma_i32_16x16x64_i8 v[6:9], v[150:153], v[190:193], 0
	s_nop 0
	v_mfma_i32_16x16x64_i8 v[6:9], v[142:145], v[186:189], v[6:9]
	v_mfma_i32_16x16x64_i8 v[10:13], v[146:149], v[190:193], 0
	s_nop 0
	v_mfma_i32_16x16x64_i8 v[10:13], v[138:141], v[186:189], v[10:13]
	v_mfma_i32_16x16x64_i8 v[14:17], v[134:137], v[190:193], 0
	s_nop 0
	v_mfma_i32_16x16x64_i8 v[14:17], v[130:133], v[186:189], v[14:17]
	v_mfma_i32_16x16x64_i8 v[30:33], v[158:161], v[182:185], 0
	s_nop 0
	v_mfma_i32_16x16x64_i8 v[30:33], v[154:157], v[178:181], v[30:33]
	v_mfma_i32_16x16x64_i8 v[42:45], v[150:153], v[182:185], 0
	s_nop 0
	v_mfma_i32_16x16x64_i8 v[42:45], v[142:145], v[178:181], v[42:45]
	v_mfma_i32_16x16x64_i8 v[38:41], v[146:149], v[182:185], 0
	s_nop 0
	v_mfma_i32_16x16x64_i8 v[38:41], v[138:141], v[178:181], v[38:41]
	v_mfma_i32_16x16x64_i8 v[46:49], v[134:137], v[182:185], 0
	s_nop 0
	v_mfma_i32_16x16x64_i8 v[46:49], v[130:133], v[178:181], v[46:49]
	v_mfma_i32_16x16x64_i8 v[58:61], v[158:161], v[174:177], 0
	s_nop 0
	v_mfma_i32_16x16x64_i8 v[58:61], v[154:157], v[170:173], v[58:61]
	v_mfma_i32_16x16x64_i8 v[74:77], v[150:153], v[174:177], 0
	s_nop 0
	v_mfma_i32_16x16x64_i8 v[74:77], v[142:145], v[170:173], v[74:77]
	v_mfma_i32_16x16x64_i8 v[70:73], v[146:149], v[174:177], 0
	s_nop 0
	v_mfma_i32_16x16x64_i8 v[70:73], v[138:141], v[170:173], v[70:73]
	v_mfma_i32_16x16x64_i8 v[78:81], v[134:137], v[174:177], 0
	s_nop 0
	v_mfma_i32_16x16x64_i8 v[78:81], v[130:133], v[170:173], v[78:81]
	v_mfma_i32_16x16x64_i8 v[90:93], v[158:161], v[166:169], 0
	s_nop 0
	v_mfma_i32_16x16x64_i8 v[90:93], v[154:157], v[162:165], v[90:93]
	v_mfma_i32_16x16x64_i8 v[106:109], v[150:153], v[166:169], 0
	s_nop 0
	v_mfma_i32_16x16x64_i8 v[106:109], v[142:145], v[162:165], v[106:109]
	v_mfma_i32_16x16x64_i8 v[102:105], v[146:149], v[166:169], 0
	s_nop 0
	v_mfma_i32_16x16x64_i8 v[102:105], v[138:141], v[162:165], v[102:105]
	v_mfma_i32_16x16x64_i8 v[110:113], v[134:137], v[166:169], 0
	s_nop 0
	v_mfma_i32_16x16x64_i8 v[110:113], v[130:133], v[162:165], v[110:113]
	s_setprio 0
	s_barrier
	s_add_u32 s45, s45, 0x100
	s_addc_u32 s78, s80, 0
	s_and_b64 s[66:67], s[76:77], exec
	s_cselect_b32 s67, s53, s78
	s_cselect_b32 s66, s52, s45
	s_add_u32 s52, s64, 0x80
	s_addc_u32 s53, s65, 0
	s_add_i32 s45, 0, 0x18000
	s_add_i32 s78, 0, 0x1c000
	v_add_u32_e32 v130, s45, v206
	v_add_u32_e32 v131, s78, v206
	ds_read_b128 v[158:161], v130
	ds_read_b128 v[154:157], v130 offset:1024
	ds_read_b128 v[150:153], v130 offset:2048
	ds_read_b128 v[146:149], v130 offset:3072
	ds_read_b128 v[142:145], v131
	ds_read_b128 v[138:141], v131 offset:1024
	ds_read_b128 v[134:137], v131 offset:2048
	ds_read_b128 v[130:133], v131 offset:3072
	s_mov_b64 s[76:77], s[66:67]
	v_mov_b32_e32 v209, v201
	s_mov_b32 m0, s1
	s_waitcnt lgkmcnt(0)
	ds_read_b128 v[162:165], v207 offset:32768
	ds_read_b128 v[166:169], v207 offset:33792
	ds_read_b128 v[170:173], v207 offset:34816
	ds_read_b128 v[174:177], v207 offset:35840
	ds_read_b128 v[178:181], v207 offset:36864
	ds_read_b128 v[182:185], v207 offset:37888
	ds_read_b128 v[186:189], v207 offset:38912
	ds_read_b128 v[190:193], v207 offset:39936
	s_add_u32 s66, s66, 0x40000
	global_load_lds_dwordx4 v209, s[76:77]
	v_mov_b32_e32 v209, v203
	s_mov_b32 m0, s61
	s_addc_u32 s67, s67, 0
	global_load_lds_dwordx4 v209, s[76:77]
	v_mov_b32_e32 v209, v201
	s_mov_b32 m0, s62
	s_nop 0
	global_load_lds_dwordx4 v209, s[66:67]
	v_mov_b32_e32 v209, v203
	s_mov_b32 m0, s63
	s_nop 0
	global_load_lds_dwordx4 v209, s[66:67]
	s_waitcnt vmcnt(8)
	s_waitcnt lgkmcnt(0)
	s_barrier
	s_setprio 1
	s_waitcnt lgkmcnt(0)
	v_mfma_i32_16x16x64_i8 v[18:21], v[158:161], v[162:165], v[18:21]
	s_nop 0
	v_mfma_i32_16x16x64_i8 v[18:21], v[154:157], v[166:169], v[18:21]
	v_mfma_i32_16x16x64_i8 v[22:25], v[150:153], v[162:165], v[22:25]
	s_nop 0
	v_mfma_i32_16x16x64_i8 v[22:25], v[146:149], v[166:169], v[22:25]
	v_mfma_i32_16x16x64_i8 v[26:29], v[142:145], v[162:165], v[26:29]
	s_nop 0
	v_mfma_i32_16x16x64_i8 v[26:29], v[138:141], v[166:169], v[26:29]
	v_mfma_i32_16x16x64_i8 v[34:37], v[134:137], v[162:165], v[34:37]
	s_nop 0
	v_mfma_i32_16x16x64_i8 v[34:37], v[130:133], v[166:169], v[34:37]
	v_mfma_i32_16x16x64_i8 v[50:53], v[158:161], v[170:173], v[50:53]
	s_nop 0
	v_mfma_i32_16x16x64_i8 v[50:53], v[154:157], v[174:177], v[50:53]
	v_mfma_i32_16x16x64_i8 v[62:65], v[150:153], v[170:173], v[62:65]
	s_nop 0
	v_mfma_i32_16x16x64_i8 v[62:65], v[146:149], v[174:177], v[62:65]
	v_mfma_i32_16x16x64_i8 v[54:57], v[142:145], v[170:173], v[54:57]
	s_nop 0
	v_mfma_i32_16x16x64_i8 v[54:57], v[138:141], v[174:177], v[54:57]
	v_mfma_i32_16x16x64_i8 v[66:69], v[134:137], v[170:173], v[66:69]
	s_nop 0
	v_mfma_i32_16x16x64_i8 v[66:69], v[130:133], v[174:177], v[66:69]
	v_mfma_i32_16x16x64_i8 v[82:85], v[158:161], v[178:181], v[82:85]
	s_nop 0
	v_mfma_i32_16x16x64_i8 v[82:85], v[154:157], v[182:185], v[82:85]
	v_mfma_i32_16x16x64_i8 v[94:97], v[150:153], v[178:181], v[94:97]
	s_nop 0
	v_mfma_i32_16x16x64_i8 v[94:97], v[146:149], v[182:185], v[94:97]
	v_mfma_i32_16x16x64_i8 v[86:89], v[142:145], v[178:181], v[86:89]
	s_nop 0
	v_mfma_i32_16x16x64_i8 v[86:89], v[138:141], v[182:185], v[86:89]
	v_mfma_i32_16x16x64_i8 v[98:101], v[134:137], v[178:181], v[98:101]
	s_nop 0
	v_mfma_i32_16x16x64_i8 v[98:101], v[130:133], v[182:185], v[98:101]
	v_mfma_i32_16x16x64_i8 v[114:117], v[158:161], v[186:189], v[114:117]
	s_nop 0
	v_mfma_i32_16x16x64_i8 v[114:117], v[154:157], v[190:193], v[114:117]
	v_mfma_i32_16x16x64_i8 v[122:125], v[150:153], v[186:189], v[122:125]
	s_nop 0
	v_mfma_i32_16x16x64_i8 v[122:125], v[146:149], v[190:193], v[122:125]
	v_mfma_i32_16x16x64_i8 v[118:121], v[142:145], v[186:189], v[118:121]
	s_nop 0
	v_mfma_i32_16x16x64_i8 v[118:121], v[138:141], v[190:193], v[118:121]
	v_mfma_i32_16x16x64_i8 v[126:129], v[134:137], v[186:189], v[126:129]
	s_nop 0
	v_mfma_i32_16x16x64_i8 v[126:129], v[130:133], v[190:193], v[126:129]
	s_setprio 0
	s_barrier
	v_mov_b32_e32 v209, v202
	s_add_i32 s45, s45, s10
	ds_read_b128 v[162:165], v207 offset:49152
	ds_read_b128 v[166:169], v207 offset:50176
	ds_read_b128 v[170:173], v207 offset:51200
	ds_read_b128 v[174:177], v207 offset:52224
	ds_read_b128 v[178:181], v207 offset:53248
	ds_read_b128 v[182:185], v207 offset:54272
	ds_read_b128 v[186:189], v207 offset:55296
	ds_read_b128 v[190:193], v207 offset:56320
	s_mov_b32 m0, s45
	s_nop 0
	global_load_lds_dwordx4 v209, s[52:53]
	v_mov_b32_e32 v209, v204
	s_add_i32 m0, s45, 0x2000
	s_nop 0
	global_load_lds_dwordx4 v209, s[52:53]
	s_add_u32 s52, s64, 0x40080
	s_addc_u32 s53, s65, 0
	v_mov_b32_e32 v209, v202
	s_add_i32 s45, s78, s10
	s_mov_b32 m0, s45
	s_nop 0
	global_load_lds_dwordx4 v209, s[52:53]
	v_mov_b32_e32 v209, v204
	s_add_i32 m0, s45, 0x2000
	s_nop 0
	global_load_lds_dwordx4 v209, s[52:53]
	s_waitcnt vmcnt(6)
	s_waitcnt lgkmcnt(0)
	s_barrier
	s_setprio 1
	s_waitcnt lgkmcnt(0)
	v_mfma_i32_16x16x64_i8 v[2:5], v[158:161], v[162:165], v[2:5]
	s_nop 0
	v_mfma_i32_16x16x64_i8 v[2:5], v[154:157], v[166:169], v[2:5]
	v_mfma_i32_16x16x64_i8 v[6:9], v[150:153], v[162:165], v[6:9]
	s_nop 0
	v_mfma_i32_16x16x64_i8 v[6:9], v[146:149], v[166:169], v[6:9]
	v_mfma_i32_16x16x64_i8 v[10:13], v[142:145], v[162:165], v[10:13]
	s_nop 0
	v_mfma_i32_16x16x64_i8 v[10:13], v[138:141], v[166:169], v[10:13]
	v_mfma_i32_16x16x64_i8 v[14:17], v[134:137], v[162:165], v[14:17]
	s_nop 0
	v_mfma_i32_16x16x64_i8 v[14:17], v[130:133], v[166:169], v[14:17]
	v_mfma_i32_16x16x64_i8 v[30:33], v[158:161], v[170:173], v[30:33]
	s_nop 0
	v_mfma_i32_16x16x64_i8 v[30:33], v[154:157], v[174:177], v[30:33]
	v_mfma_i32_16x16x64_i8 v[42:45], v[150:153], v[170:173], v[42:45]
	s_nop 0
	v_mfma_i32_16x16x64_i8 v[42:45], v[146:149], v[174:177], v[42:45]
	v_mfma_i32_16x16x64_i8 v[38:41], v[142:145], v[170:173], v[38:41]
	s_nop 0
	v_mfma_i32_16x16x64_i8 v[38:41], v[138:141], v[174:177], v[38:41]
	v_mfma_i32_16x16x64_i8 v[46:49], v[134:137], v[170:173], v[46:49]
	s_nop 0
	v_mfma_i32_16x16x64_i8 v[46:49], v[130:133], v[174:177], v[46:49]
	v_mfma_i32_16x16x64_i8 v[58:61], v[158:161], v[178:181], v[58:61]
	s_nop 0
	v_mfma_i32_16x16x64_i8 v[58:61], v[154:157], v[182:185], v[58:61]
	v_mfma_i32_16x16x64_i8 v[74:77], v[150:153], v[178:181], v[74:77]
	s_nop 0
	v_mfma_i32_16x16x64_i8 v[74:77], v[146:149], v[182:185], v[74:77]
	v_mfma_i32_16x16x64_i8 v[70:73], v[142:145], v[178:181], v[70:73]
	s_nop 0
	v_mfma_i32_16x16x64_i8 v[70:73], v[138:141], v[182:185], v[70:73]
	v_mfma_i32_16x16x64_i8 v[78:81], v[134:137], v[178:181], v[78:81]
	s_nop 0
	v_mfma_i32_16x16x64_i8 v[78:81], v[130:133], v[182:185], v[78:81]
	v_mfma_i32_16x16x64_i8 v[90:93], v[158:161], v[186:189], v[90:93]
	s_nop 0
	v_mfma_i32_16x16x64_i8 v[90:93], v[154:157], v[190:193], v[90:93]
	v_mfma_i32_16x16x64_i8 v[106:109], v[150:153], v[186:189], v[106:109]
	s_nop 0
	v_mfma_i32_16x16x64_i8 v[106:109], v[146:149], v[190:193], v[106:109]
	v_mfma_i32_16x16x64_i8 v[102:105], v[142:145], v[186:189], v[102:105]
	s_nop 0
	v_mfma_i32_16x16x64_i8 v[102:105], v[138:141], v[190:193], v[102:105]
	v_mfma_i32_16x16x64_i8 v[110:113], v[134:137], v[186:189], v[110:113]
	s_nop 0
	v_mfma_i32_16x16x64_i8 v[110:113], v[130:133], v[190:193], v[110:113]
	s_setprio 0
	s_barrier
	s_add_i32 s43, s43, 2
	s_add_u32 s50, s50, 0x100
	s_addc_u32 s51, s51, 0
	s_cmp_gt_u32 s43, 13
	s_cbranch_scc1 .LBB0_861
	s_mov_b64 s[64:65], s[8:9]
	s_mov_b64 s[52:53], s[26:27]

.Li8b_851_847:
	s_waitcnt vmcnt(8)
	s_waitcnt lgkmcnt(0)
	s_barrier
	s_setprio 1
	v_mfma_i32_16x16x64_i8 v[18:21], v[158:161], v[190:193], v[18:21]
	s_nop 0
	v_mfma_i32_16x16x64_i8 v[18:21], v[154:157], v[186:189], v[18:21]
	v_mfma_i32_16x16x64_i8 v[22:25], v[150:153], v[190:193], v[22:25]
	s_nop 0
	v_mfma_i32_16x16x64_i8 v[22:25], v[142:145], v[186:189], v[22:25]
	v_mfma_i32_16x16x64_i8 v[26:29], v[146:149], v[190:193], v[26:29]
	s_nop 0
	v_mfma_i32_16x16x64_i8 v[26:29], v[138:141], v[186:189], v[26:29]
	v_mfma_i32_16x16x64_i8 v[34:37], v[134:137], v[190:193], v[34:37]
	s_nop 0
	v_mfma_i32_16x16x64_i8 v[34:37], v[130:133], v[186:189], v[34:37]
	v_mfma_i32_16x16x64_i8 v[50:53], v[158:161], v[182:185], v[50:53]
	s_nop 0
	v_mfma_i32_16x16x64_i8 v[50:53], v[154:157], v[178:181], v[50:53]
	v_mfma_i32_16x16x64_i8 v[62:65], v[150:153], v[182:185], v[62:65]
	s_nop 0
	v_mfma_i32_16x16x64_i8 v[62:65], v[142:145], v[178:181], v[62:65]
	v_mfma_i32_16x16x64_i8 v[54:57], v[146:149], v[182:185], v[54:57]
	s_nop 0
	v_mfma_i32_16x16x64_i8 v[54:57], v[138:141], v[178:181], v[54:57]
	v_mfma_i32_16x16x64_i8 v[66:69], v[134:137], v[182:185], v[66:69]
	s_nop 0
	v_mfma_i32_16x16x64_i8 v[66:69], v[130:133], v[178:181], v[66:69]
	v_mfma_i32_16x16x64_i8 v[82:85], v[158:161], v[174:177], v[82:85]
	s_nop 0
	v_mfma_i32_16x16x64_i8 v[82:85], v[154:157], v[170:173], v[82:85]
	v_mfma_i32_16x16x64_i8 v[94:97], v[150:153], v[174:177], v[94:97]
	s_nop 0
	v_mfma_i32_16x16x64_i8 v[94:97], v[142:145], v[170:173], v[94:97]
	v_mfma_i32_16x16x64_i8 v[86:89], v[146:149], v[174:177], v[86:89]
	s_nop 0
	v_mfma_i32_16x16x64_i8 v[86:89], v[138:141], v[170:173], v[86:89]
	v_mfma_i32_16x16x64_i8 v[98:101], v[134:137], v[174:177], v[98:101]
	s_nop 0
	v_mfma_i32_16x16x64_i8 v[98:101], v[130:133], v[170:173], v[98:101]
	v_mfma_i32_16x16x64_i8 v[114:117], v[158:161], v[166:169], v[114:117]
	s_nop 0
	v_mfma_i32_16x16x64_i8 v[114:117], v[154:157], v[162:165], v[114:117]
	v_mfma_i32_16x16x64_i8 v[122:125], v[150:153], v[166:169], v[122:125]
	s_nop 0
	v_mfma_i32_16x16x64_i8 v[122:125], v[142:145], v[162:165], v[122:125]
	v_mfma_i32_16x16x64_i8 v[118:121], v[146:149], v[166:169], v[118:121]
	s_nop 0
	v_mfma_i32_16x16x64_i8 v[118:121], v[138:141], v[162:165], v[118:121]
	v_mfma_i32_16x16x64_i8 v[126:129], v[134:137], v[166:169], v[126:129]
	s_nop 0
	v_mfma_i32_16x16x64_i8 v[126:129], v[130:133], v[162:165], v[126:129]
	s_setprio 0
	s_barrier
	s_add_u32 s81, s74, s50
	s_addc_u32 s82, s75, s51
	s_cmp_eq_u32 s43, 12
	s_cselect_b64 s[76:77], -1, 0
	s_and_b64 s[78:79], s[76:77], exec
	s_cselect_b32 s65, s65, s82
	s_cselect_b32 s64, s64, s81
	s_mov_b64 s[78:79], s[64:65]
	v_mov_b32_e32 v209, v202
	s_mov_b32 m0, s21
	s_waitcnt lgkmcnt(0)
	ds_read_b128 v[190:193], v207 offset:16384
	ds_read_b128 v[186:189], v207 offset:17408
	ds_read_b128 v[182:185], v207 offset:18432
	ds_read_b128 v[178:181], v207 offset:19456
	ds_read_b128 v[174:177], v207 offset:20480
	ds_read_b128 v[170:173], v207 offset:21504
	ds_read_b128 v[166:169], v207 offset:22528
	ds_read_b128 v[162:165], v207 offset:23552
	s_nop 0
	global_load_lds_dwordx4 v209, s[78:79]
	v_mov_b32_e32 v209, v204
	s_mov_b32 m0, s33
	s_nop 0
	global_load_lds_dwordx4 v209, s[78:79]
	s_add_u32 s78, s64, 0x40000
	s_addc_u32 s79, s65, 0
	v_mov_b32_e32 v209, v202
	s_mov_b32 m0, s35
	s_nop 0
	global_load_lds_dwordx4 v209, s[78:79]
	v_mov_b32_e32 v209, v204
	s_mov_b32 m0, s60
	s_nop 0
	global_load_lds_dwordx4 v209, s[78:79]
	s_waitcnt vmcnt(6)
	s_waitcnt lgkmcnt(0)
	s_barrier
	s_setprio 1
	v_mfma_i32_16x16x64_i8 v[2:5], v[158:161], v[190:193], v[2:5]
	s_nop 0
	v_mfma_i32_16x16x64_i8 v[2:5], v[154:157], v[186:189], v[2:5]
	v_mfma_i32_16x16x64_i8 v[6:9], v[150:153], v[190:193], v[6:9]
	s_nop 0
	v_mfma_i32_16x16x64_i8 v[6:9], v[142:145], v[186:189], v[6:9]
	v_mfma_i32_16x16x64_i8 v[10:13], v[146:149], v[190:193], v[10:13]
	s_nop 0
	v_mfma_i32_16x16x64_i8 v[10:13], v[138:141], v[186:189], v[10:13]
	v_mfma_i32_16x16x64_i8 v[14:17], v[134:137], v[190:193], v[14:17]
	s_nop 0
	v_mfma_i32_16x16x64_i8 v[14:17], v[130:133], v[186:189], v[14:17]
	v_mfma_i32_16x16x64_i8 v[30:33], v[158:161], v[182:185], v[30:33]
	s_nop 0
	v_mfma_i32_16x16x64_i8 v[30:33], v[154:157], v[178:181], v[30:33]
	v_mfma_i32_16x16x64_i8 v[42:45], v[150:153], v[182:185], v[42:45]
	s_nop 0
	v_mfma_i32_16x16x64_i8 v[42:45], v[142:145], v[178:181], v[42:45]
	v_mfma_i32_16x16x64_i8 v[38:41], v[146:149], v[182:185], v[38:41]
	s_nop 0
	v_mfma_i32_16x16x64_i8 v[38:41], v[138:141], v[178:181], v[38:41]
	v_mfma_i32_16x16x64_i8 v[46:49], v[134:137], v[182:185], v[46:49]
	s_nop 0
	v_mfma_i32_16x16x64_i8 v[46:49], v[130:133], v[178:181], v[46:49]
	v_mfma_i32_16x16x64_i8 v[58:61], v[158:161], v[174:177], v[58:61]
	s_nop 0
	v_mfma_i32_16x16x64_i8 v[58:61], v[154:157], v[170:173], v[58:61]
	v_mfma_i32_16x16x64_i8 v[74:77], v[150:153], v[174:177], v[74:77]
	s_nop 0
	v_mfma_i32_16x16x64_i8 v[74:77], v[142:145], v[170:173], v[74:77]
	v_mfma_i32_16x16x64_i8 v[70:73], v[146:149], v[174:177], v[70:73]
	s_nop 0
	v_mfma_i32_16x16x64_i8 v[70:73], v[138:141], v[170:173], v[70:73]
	v_mfma_i32_16x16x64_i8 v[78:81], v[134:137], v[174:177], v[78:81]
	s_nop 0
	v_mfma_i32_16x16x64_i8 v[78:81], v[130:133], v[170:173], v[78:81]
	v_mfma_i32_16x16x64_i8 v[90:93], v[158:161], v[166:169], v[90:93]
	s_nop 0
	v_mfma_i32_16x16x64_i8 v[90:93], v[154:157], v[162:165], v[90:93]
	v_mfma_i32_16x16x64_i8 v[106:109], v[150:153], v[166:169], v[106:109]
	s_nop 0
	v_mfma_i32_16x16x64_i8 v[106:109], v[142:145], v[162:165], v[106:109]
	v_mfma_i32_16x16x64_i8 v[102:105], v[146:149], v[166:169], v[102:105]
	s_nop 0
	v_mfma_i32_16x16x64_i8 v[102:105], v[138:141], v[162:165], v[102:105]
	v_mfma_i32_16x16x64_i8 v[110:113], v[134:137], v[166:169], v[110:113]
	s_nop 0
	v_mfma_i32_16x16x64_i8 v[110:113], v[130:133], v[162:165], v[110:113]
	s_setprio 0
	s_barrier
	s_add_u32 s45, s45, 0x100
	s_addc_u32 s78, s80, 0
	s_and_b64 s[66:67], s[76:77], exec
	s_cselect_b32 s67, s53, s78
	s_cselect_b32 s66, s52, s45
	s_add_u32 s52, s64, 0x80
	s_addc_u32 s53, s65, 0
	s_add_i32 s45, 0, 0x18000
	s_add_i32 s78, 0, 0x1c000
	v_add_u32_e32 v130, s45, v206
	v_add_u32_e32 v131, s78, v206
	ds_read_b128 v[158:161], v130
	ds_read_b128 v[154:157], v130 offset:1024
	ds_read_b128 v[150:153], v130 offset:2048
	ds_read_b128 v[146:149], v130 offset:3072
	ds_read_b128 v[142:145], v131
	ds_read_b128 v[138:141], v131 offset:1024
	ds_read_b128 v[134:137], v131 offset:2048
	ds_read_b128 v[130:133], v131 offset:3072
	s_mov_b64 s[76:77], s[66:67]
	v_mov_b32_e32 v209, v201
	s_mov_b32 m0, s1
	s_waitcnt lgkmcnt(0)
	ds_read_b128 v[162:165], v207 offset:32768
	ds_read_b128 v[166:169], v207 offset:33792
	ds_read_b128 v[170:173], v207 offset:34816
	ds_read_b128 v[174:177], v207 offset:35840
	ds_read_b128 v[178:181], v207 offset:36864
	ds_read_b128 v[182:185], v207 offset:37888
	ds_read_b128 v[186:189], v207 offset:38912
	ds_read_b128 v[190:193], v207 offset:39936
	s_add_u32 s66, s66, 0x40000
	global_load_lds_dwordx4 v209, s[76:77]
	v_mov_b32_e32 v209, v203
	s_mov_b32 m0, s61
	s_addc_u32 s67, s67, 0
	global_load_lds_dwordx4 v209, s[76:77]
	v_mov_b32_e32 v209, v201
	s_mov_b32 m0, s62
	s_nop 0
	global_load_lds_dwordx4 v209, s[66:67]
	v_mov_b32_e32 v209, v203
	s_mov_b32 m0, s63
	s_nop 0
	global_load_lds_dwordx4 v209, s[66:67]
	s_waitcnt vmcnt(8)
	s_waitcnt lgkmcnt(0)
	s_barrier
	s_setprio 1
	s_waitcnt lgkmcnt(0)
	v_mfma_i32_16x16x64_i8 v[18:21], v[158:161], v[162:165], v[18:21]
	s_nop 0
	v_mfma_i32_16x16x64_i8 v[18:21], v[154:157], v[166:169], v[18:21]
	v_mfma_i32_16x16x64_i8 v[22:25], v[150:153], v[162:165], v[22:25]
	s_nop 0
	v_mfma_i32_16x16x64_i8 v[22:25], v[146:149], v[166:169], v[22:25]
	v_mfma_i32_16x16x64_i8 v[26:29], v[142:145], v[162:165], v[26:29]
	s_nop 0
	v_mfma_i32_16x16x64_i8 v[26:29], v[138:141], v[166:169], v[26:29]
	v_mfma_i32_16x16x64_i8 v[34:37], v[134:137], v[162:165], v[34:37]
	s_nop 0
	v_mfma_i32_16x16x64_i8 v[34:37], v[130:133], v[166:169], v[34:37]
	v_mfma_i32_16x16x64_i8 v[50:53], v[158:161], v[170:173], v[50:53]
	s_nop 0
	v_mfma_i32_16x16x64_i8 v[50:53], v[154:157], v[174:177], v[50:53]
	v_mfma_i32_16x16x64_i8 v[62:65], v[150:153], v[170:173], v[62:65]
	s_nop 0
	v_mfma_i32_16x16x64_i8 v[62:65], v[146:149], v[174:177], v[62:65]
	v_mfma_i32_16x16x64_i8 v[54:57], v[142:145], v[170:173], v[54:57]
	s_nop 0
	v_mfma_i32_16x16x64_i8 v[54:57], v[138:141], v[174:177], v[54:57]
	v_mfma_i32_16x16x64_i8 v[66:69], v[134:137], v[170:173], v[66:69]
	s_nop 0
	v_mfma_i32_16x16x64_i8 v[66:69], v[130:133], v[174:177], v[66:69]
	v_mfma_i32_16x16x64_i8 v[82:85], v[158:161], v[178:181], v[82:85]
	s_nop 0
	v_mfma_i32_16x16x64_i8 v[82:85], v[154:157], v[182:185], v[82:85]
	v_mfma_i32_16x16x64_i8 v[94:97], v[150:153], v[178:181], v[94:97]
	s_nop 0
	v_mfma_i32_16x16x64_i8 v[94:97], v[146:149], v[182:185], v[94:97]
	v_mfma_i32_16x16x64_i8 v[86:89], v[142:145], v[178:181], v[86:89]
	s_nop 0
	v_mfma_i32_16x16x64_i8 v[86:89], v[138:141], v[182:185], v[86:89]
	v_mfma_i32_16x16x64_i8 v[98:101], v[134:137], v[178:181], v[98:101]
	s_nop 0
	v_mfma_i32_16x16x64_i8 v[98:101], v[130:133], v[182:185], v[98:101]
	v_mfma_i32_16x16x64_i8 v[114:117], v[158:161], v[186:189], v[114:117]
	s_nop 0
	v_mfma_i32_16x16x64_i8 v[114:117], v[154:157], v[190:193], v[114:117]
	v_mfma_i32_16x16x64_i8 v[122:125], v[150:153], v[186:189], v[122:125]
	s_nop 0
	v_mfma_i32_16x16x64_i8 v[122:125], v[146:149], v[190:193], v[122:125]
	v_mfma_i32_16x16x64_i8 v[118:121], v[142:145], v[186:189], v[118:121]
	s_nop 0
	v_mfma_i32_16x16x64_i8 v[118:121], v[138:141], v[190:193], v[118:121]
	v_mfma_i32_16x16x64_i8 v[126:129], v[134:137], v[186:189], v[126:129]
	s_nop 0
	v_mfma_i32_16x16x64_i8 v[126:129], v[130:133], v[190:193], v[126:129]
	s_setprio 0
	s_barrier
	v_mov_b32_e32 v209, v202
	s_add_i32 s45, s45, s10
	ds_read_b128 v[162:165], v207 offset:49152
	ds_read_b128 v[166:169], v207 offset:50176
	ds_read_b128 v[170:173], v207 offset:51200
	ds_read_b128 v[174:177], v207 offset:52224
	ds_read_b128 v[178:181], v207 offset:53248
	ds_read_b128 v[182:185], v207 offset:54272
	ds_read_b128 v[186:189], v207 offset:55296
	ds_read_b128 v[190:193], v207 offset:56320
	s_mov_b32 m0, s45
	s_nop 0
	global_load_lds_dwordx4 v209, s[52:53]
	v_mov_b32_e32 v209, v204
	s_add_i32 m0, s45, 0x2000
	s_nop 0
	global_load_lds_dwordx4 v209, s[52:53]
	s_add_u32 s52, s64, 0x40080
	s_addc_u32 s53, s65, 0
	v_mov_b32_e32 v209, v202
	s_add_i32 s45, s78, s10
	s_mov_b32 m0, s45
	s_nop 0
	global_load_lds_dwordx4 v209, s[52:53]
	v_mov_b32_e32 v209, v204
	s_add_i32 m0, s45, 0x2000
	s_nop 0
	global_load_lds_dwordx4 v209, s[52:53]
	s_waitcnt vmcnt(6)
	s_waitcnt lgkmcnt(0)
	s_barrier
	s_setprio 1
	s_waitcnt lgkmcnt(0)
	v_mfma_i32_16x16x64_i8 v[2:5], v[158:161], v[162:165], v[2:5]
	s_nop 0
	v_mfma_i32_16x16x64_i8 v[2:5], v[154:157], v[166:169], v[2:5]
	v_mfma_i32_16x16x64_i8 v[6:9], v[150:153], v[162:165], v[6:9]
	s_nop 0
	v_mfma_i32_16x16x64_i8 v[6:9], v[146:149], v[166:169], v[6:9]
	v_mfma_i32_16x16x64_i8 v[10:13], v[142:145], v[162:165], v[10:13]
	s_nop 0
	v_mfma_i32_16x16x64_i8 v[10:13], v[138:141], v[166:169], v[10:13]
	v_mfma_i32_16x16x64_i8 v[14:17], v[134:137], v[162:165], v[14:17]
	s_nop 0
	v_mfma_i32_16x16x64_i8 v[14:17], v[130:133], v[166:169], v[14:17]
	v_mfma_i32_16x16x64_i8 v[30:33], v[158:161], v[170:173], v[30:33]
	s_nop 0
	v_mfma_i32_16x16x64_i8 v[30:33], v[154:157], v[174:177], v[30:33]
	v_mfma_i32_16x16x64_i8 v[42:45], v[150:153], v[170:173], v[42:45]
	s_nop 0
	v_mfma_i32_16x16x64_i8 v[42:45], v[146:149], v[174:177], v[42:45]
	v_mfma_i32_16x16x64_i8 v[38:41], v[142:145], v[170:173], v[38:41]
	s_nop 0
	v_mfma_i32_16x16x64_i8 v[38:41], v[138:141], v[174:177], v[38:41]
	v_mfma_i32_16x16x64_i8 v[46:49], v[134:137], v[170:173], v[46:49]
	s_nop 0
	v_mfma_i32_16x16x64_i8 v[46:49], v[130:133], v[174:177], v[46:49]
	v_mfma_i32_16x16x64_i8 v[58:61], v[158:161], v[178:181], v[58:61]
	s_nop 0
	v_mfma_i32_16x16x64_i8 v[58:61], v[154:157], v[182:185], v[58:61]
	v_mfma_i32_16x16x64_i8 v[74:77], v[150:153], v[178:181], v[74:77]
	s_nop 0
	v_mfma_i32_16x16x64_i8 v[74:77], v[146:149], v[182:185], v[74:77]
	v_mfma_i32_16x16x64_i8 v[70:73], v[142:145], v[178:181], v[70:73]
	s_nop 0
	v_mfma_i32_16x16x64_i8 v[70:73], v[138:141], v[182:185], v[70:73]
	v_mfma_i32_16x16x64_i8 v[78:81], v[134:137], v[178:181], v[78:81]
	s_nop 0
	v_mfma_i32_16x16x64_i8 v[78:81], v[130:133], v[182:185], v[78:81]
	v_mfma_i32_16x16x64_i8 v[90:93], v[158:161], v[186:189], v[90:93]
	s_nop 0
	v_mfma_i32_16x16x64_i8 v[90:93], v[154:157], v[190:193], v[90:93]
	v_mfma_i32_16x16x64_i8 v[106:109], v[150:153], v[186:189], v[106:109]
	s_nop 0
	v_mfma_i32_16x16x64_i8 v[106:109], v[146:149], v[190:193], v[106:109]
	v_mfma_i32_16x16x64_i8 v[102:105], v[142:145], v[186:189], v[102:105]
	s_nop 0
	v_mfma_i32_16x16x64_i8 v[102:105], v[138:141], v[190:193], v[102:105]
	v_mfma_i32_16x16x64_i8 v[110:113], v[134:137], v[186:189], v[110:113]
	s_nop 0
	v_mfma_i32_16x16x64_i8 v[110:113], v[130:133], v[190:193], v[110:113]
	s_setprio 0
	s_barrier
	s_add_i32 s43, s43, 2
	s_add_u32 s50, s50, 0x100
	s_addc_u32 s51, s51, 0
	s_cmp_gt_u32 s43, 13
	s_cbranch_scc1 .LBB0_861
	s_mov_b64 s[64:65], s[8:9]
	s_mov_b64 s[52:53], s[26:27]
	s_branch .Li8loop_847

.LBB0_1088:
	s_waitcnt vmcnt(8)
	s_waitcnt lgkmcnt(0)
	s_barrier
	s_setprio 1
	v_mfma_i32_16x16x64_i8 v[18:21], v[158:161], v[190:193], 0
	s_nop 0
	v_mfma_i32_16x16x64_i8 v[18:21], v[154:157], v[186:189], v[18:21]
	v_mfma_i32_16x16x64_i8 v[22:25], v[150:153], v[190:193], 0
	s_nop 0
	v_mfma_i32_16x16x64_i8 v[22:25], v[142:145], v[186:189], v[22:25]
	v_mfma_i32_16x16x64_i8 v[26:29], v[146:149], v[190:193], 0
	s_nop 0
	v_mfma_i32_16x16x64_i8 v[26:29], v[138:141], v[186:189], v[26:29]
	v_mfma_i32_16x16x64_i8 v[34:37], v[134:137], v[190:193], 0
	s_nop 0
	v_mfma_i32_16x16x64_i8 v[34:37], v[130:133], v[186:189], v[34:37]
	v_mfma_i32_16x16x64_i8 v[50:53], v[158:161], v[182:185], 0
	s_nop 0
	v_mfma_i32_16x16x64_i8 v[50:53], v[154:157], v[178:181], v[50:53]
	v_mfma_i32_16x16x64_i8 v[62:65], v[150:153], v[182:185], 0
	s_nop 0
	v_mfma_i32_16x16x64_i8 v[62:65], v[142:145], v[178:181], v[62:65]
	v_mfma_i32_16x16x64_i8 v[54:57], v[146:149], v[182:185], 0
	s_nop 0
	v_mfma_i32_16x16x64_i8 v[54:57], v[138:141], v[178:181], v[54:57]
	v_mfma_i32_16x16x64_i8 v[66:69], v[134:137], v[182:185], 0
	s_nop 0
	v_mfma_i32_16x16x64_i8 v[66:69], v[130:133], v[178:181], v[66:69]
	v_mfma_i32_16x16x64_i8 v[82:85], v[158:161], v[174:177], 0
	s_nop 0
	v_mfma_i32_16x16x64_i8 v[82:85], v[154:157], v[170:173], v[82:85]
	v_mfma_i32_16x16x64_i8 v[94:97], v[150:153], v[174:177], 0
	s_nop 0
	v_mfma_i32_16x16x64_i8 v[94:97], v[142:145], v[170:173], v[94:97]
	v_mfma_i32_16x16x64_i8 v[86:89], v[146:149], v[174:177], 0
	s_nop 0
	v_mfma_i32_16x16x64_i8 v[86:89], v[138:141], v[170:173], v[86:89]
	v_mfma_i32_16x16x64_i8 v[98:101], v[134:137], v[174:177], 0
	s_nop 0
	v_mfma_i32_16x16x64_i8 v[98:101], v[130:133], v[170:173], v[98:101]
	v_mfma_i32_16x16x64_i8 v[114:117], v[158:161], v[166:169], 0
	s_nop 0
	v_mfma_i32_16x16x64_i8 v[114:117], v[154:157], v[162:165], v[114:117]
	v_mfma_i32_16x16x64_i8 v[122:125], v[150:153], v[166:169], 0
	s_nop 0
	v_mfma_i32_16x16x64_i8 v[122:125], v[142:145], v[162:165], v[122:125]
	v_mfma_i32_16x16x64_i8 v[118:121], v[146:149], v[166:169], 0
	s_nop 0
	v_mfma_i32_16x16x64_i8 v[118:121], v[138:141], v[162:165], v[118:121]
	v_mfma_i32_16x16x64_i8 v[126:129], v[134:137], v[166:169], 0
	s_nop 0
	v_mfma_i32_16x16x64_i8 v[126:129], v[130:133], v[162:165], v[126:129]
	s_setprio 0
	s_barrier
	s_add_u32 s81, s77, s48
	s_addc_u32 s82, s78, s49
	s_cmp_eq_u32 s41, 12
	s_cselect_b64 s[66:67], -1, 0
	s_and_b64 s[74:75], s[66:67], exec
	s_cselect_b32 s53, s53, s82
	s_cselect_b32 s52, s52, s81
	s_mov_b64 s[74:75], s[52:53]
	v_mov_b32_e32 v205, v197
	s_mov_b32 m0, s33
	s_waitcnt lgkmcnt(0)
	ds_read_b128 v[190:193], v204 offset:16384
	ds_read_b128 v[186:189], v204 offset:17408
	ds_read_b128 v[182:185], v204 offset:18432
	ds_read_b128 v[178:181], v204 offset:19456
	ds_read_b128 v[174:177], v204 offset:20480
	ds_read_b128 v[170:173], v204 offset:21504
	ds_read_b128 v[166:169], v204 offset:22528
	ds_read_b128 v[162:165], v204 offset:23552
	s_nop 0
	global_load_lds_dwordx4 v205, s[74:75]
	v_mov_b32_e32 v205, v199
	s_mov_b32 m0, s35
	s_nop 0
	global_load_lds_dwordx4 v205, s[74:75]
	s_add_u32 s74, s52, 0x40000
	s_addc_u32 s75, s53, 0
	v_mov_b32_e32 v205, v197
	s_mov_b32 m0, s60
	s_nop 0
	global_load_lds_dwordx4 v205, s[74:75]
	v_mov_b32_e32 v205, v199
	s_mov_b32 m0, s61
	s_nop 0
	global_load_lds_dwordx4 v205, s[74:75]
	s_waitcnt vmcnt(6)
	s_waitcnt lgkmcnt(0)
	s_barrier
	s_setprio 1
	v_mfma_i32_16x16x64_i8 v[2:5], v[158:161], v[190:193], 0
	s_nop 0
	v_mfma_i32_16x16x64_i8 v[2:5], v[154:157], v[186:189], v[2:5]
	v_mfma_i32_16x16x64_i8 v[6:9], v[150:153], v[190:193], 0
	s_nop 0
	v_mfma_i32_16x16x64_i8 v[6:9], v[142:145], v[186:189], v[6:9]
	v_mfma_i32_16x16x64_i8 v[10:13], v[146:149], v[190:193], 0
	s_nop 0
	v_mfma_i32_16x16x64_i8 v[10:13], v[138:141], v[186:189], v[10:13]
	v_mfma_i32_16x16x64_i8 v[14:17], v[134:137], v[190:193], 0
	s_nop 0
	v_mfma_i32_16x16x64_i8 v[14:17], v[130:133], v[186:189], v[14:17]
	v_mfma_i32_16x16x64_i8 v[30:33], v[158:161], v[182:185], 0
	s_nop 0
	v_mfma_i32_16x16x64_i8 v[30:33], v[154:157], v[178:181], v[30:33]
	v_mfma_i32_16x16x64_i8 v[42:45], v[150:153], v[182:185], 0
	s_nop 0
	v_mfma_i32_16x16x64_i8 v[42:45], v[142:145], v[178:181], v[42:45]
	v_mfma_i32_16x16x64_i8 v[38:41], v[146:149], v[182:185], 0
	s_nop 0
	v_mfma_i32_16x16x64_i8 v[38:41], v[138:141], v[178:181], v[38:41]
	v_mfma_i32_16x16x64_i8 v[46:49], v[134:137], v[182:185], 0
	s_nop 0
	v_mfma_i32_16x16x64_i8 v[46:49], v[130:133], v[178:181], v[46:49]
	v_mfma_i32_16x16x64_i8 v[58:61], v[158:161], v[174:177], 0
	s_nop 0
	v_mfma_i32_16x16x64_i8 v[58:61], v[154:157], v[170:173], v[58:61]
	v_mfma_i32_16x16x64_i8 v[74:77], v[150:153], v[174:177], 0
	s_nop 0
	v_mfma_i32_16x16x64_i8 v[74:77], v[142:145], v[170:173], v[74:77]
	v_mfma_i32_16x16x64_i8 v[70:73], v[146:149], v[174:177], 0
	s_nop 0
	v_mfma_i32_16x16x64_i8 v[70:73], v[138:141], v[170:173], v[70:73]
	v_mfma_i32_16x16x64_i8 v[78:81], v[134:137], v[174:177], 0
	s_nop 0
	v_mfma_i32_16x16x64_i8 v[78:81], v[130:133], v[170:173], v[78:81]
	v_mfma_i32_16x16x64_i8 v[90:93], v[158:161], v[166:169], 0
	s_nop 0
	v_mfma_i32_16x16x64_i8 v[90:93], v[154:157], v[162:165], v[90:93]
	v_mfma_i32_16x16x64_i8 v[106:109], v[150:153], v[166:169], 0
	s_nop 0
	v_mfma_i32_16x16x64_i8 v[106:109], v[142:145], v[162:165], v[106:109]
	v_mfma_i32_16x16x64_i8 v[102:105], v[146:149], v[166:169], 0
	s_nop 0
	v_mfma_i32_16x16x64_i8 v[102:105], v[138:141], v[162:165], v[102:105]
	v_mfma_i32_16x16x64_i8 v[110:113], v[134:137], v[166:169], 0
	s_nop 0
	v_mfma_i32_16x16x64_i8 v[110:113], v[130:133], v[162:165], v[110:113]
	s_setprio 0
	s_barrier
	s_add_u32 s43, s43, 0x100
	s_addc_u32 s74, s80, 0
	s_and_b64 s[64:65], s[66:67], exec
	s_cselect_b32 s65, s51, s74
	s_cselect_b32 s64, s50, s43
	s_add_u32 s50, s52, 0x80
	s_addc_u32 s51, s53, 0
	s_add_i32 s43, 0, 0x18000
	s_add_i32 s74, 0, 0x1c000
	v_add_u32_e32 v130, s43, v202
	v_add_u32_e32 v131, s74, v202
	ds_read_b128 v[158:161], v130
	ds_read_b128 v[154:157], v130 offset:1024
	ds_read_b128 v[150:153], v130 offset:2048
	ds_read_b128 v[146:149], v130 offset:3072
	ds_read_b128 v[142:145], v131
	ds_read_b128 v[138:141], v131 offset:1024
	ds_read_b128 v[134:137], v131 offset:2048
	ds_read_b128 v[130:133], v131 offset:3072
	s_mov_b64 s[66:67], s[64:65]
	v_mov_b32_e32 v205, v196
	s_mov_b32 m0, s5
	s_waitcnt lgkmcnt(0)
	ds_read_b128 v[162:165], v204 offset:32768
	ds_read_b128 v[166:169], v204 offset:33792
	ds_read_b128 v[170:173], v204 offset:34816
	ds_read_b128 v[174:177], v204 offset:35840
	ds_read_b128 v[178:181], v204 offset:36864
	ds_read_b128 v[182:185], v204 offset:37888
	ds_read_b128 v[186:189], v204 offset:38912
	ds_read_b128 v[190:193], v204 offset:39936
	s_add_u32 s64, s64, 0x40000
	global_load_lds_dwordx4 v205, s[66:67]
	v_mov_b32_e32 v205, v198
	s_mov_b32 m0, s62
	s_addc_u32 s65, s65, 0
	global_load_lds_dwordx4 v205, s[66:67]
	v_mov_b32_e32 v205, v196
	s_mov_b32 m0, s63
	s_nop 0
	global_load_lds_dwordx4 v205, s[64:65]
	v_mov_b32_e32 v205, v198
	s_mov_b32 m0, s69
	s_nop 0
	global_load_lds_dwordx4 v205, s[64:65]
	s_waitcnt vmcnt(8)
	s_waitcnt lgkmcnt(0)
	s_barrier
	s_setprio 1
	s_waitcnt lgkmcnt(0)
	v_mfma_i32_16x16x64_i8 v[18:21], v[158:161], v[162:165], v[18:21]
	s_nop 0
	v_mfma_i32_16x16x64_i8 v[18:21], v[154:157], v[166:169], v[18:21]
	v_mfma_i32_16x16x64_i8 v[22:25], v[150:153], v[162:165], v[22:25]
	s_nop 0
	v_mfma_i32_16x16x64_i8 v[22:25], v[146:149], v[166:169], v[22:25]
	v_mfma_i32_16x16x64_i8 v[26:29], v[142:145], v[162:165], v[26:29]
	s_nop 0
	v_mfma_i32_16x16x64_i8 v[26:29], v[138:141], v[166:169], v[26:29]
	v_mfma_i32_16x16x64_i8 v[34:37], v[134:137], v[162:165], v[34:37]
	s_nop 0
	v_mfma_i32_16x16x64_i8 v[34:37], v[130:133], v[166:169], v[34:37]
	v_mfma_i32_16x16x64_i8 v[50:53], v[158:161], v[170:173], v[50:53]
	s_nop 0
	v_mfma_i32_16x16x64_i8 v[50:53], v[154:157], v[174:177], v[50:53]
	v_mfma_i32_16x16x64_i8 v[62:65], v[150:153], v[170:173], v[62:65]
	s_nop 0
	v_mfma_i32_16x16x64_i8 v[62:65], v[146:149], v[174:177], v[62:65]
	v_mfma_i32_16x16x64_i8 v[54:57], v[142:145], v[170:173], v[54:57]
	s_nop 0
	v_mfma_i32_16x16x64_i8 v[54:57], v[138:141], v[174:177], v[54:57]
	v_mfma_i32_16x16x64_i8 v[66:69], v[134:137], v[170:173], v[66:69]
	s_nop 0
	v_mfma_i32_16x16x64_i8 v[66:69], v[130:133], v[174:177], v[66:69]
	v_mfma_i32_16x16x64_i8 v[82:85], v[158:161], v[178:181], v[82:85]
	s_nop 0
	v_mfma_i32_16x16x64_i8 v[82:85], v[154:157], v[182:185], v[82:85]
	v_mfma_i32_16x16x64_i8 v[94:97], v[150:153], v[178:181], v[94:97]
	s_nop 0
	v_mfma_i32_16x16x64_i8 v[94:97], v[146:149], v[182:185], v[94:97]
	v_mfma_i32_16x16x64_i8 v[86:89], v[142:145], v[178:181], v[86:89]
	s_nop 0
	v_mfma_i32_16x16x64_i8 v[86:89], v[138:141], v[182:185], v[86:89]
	v_mfma_i32_16x16x64_i8 v[98:101], v[134:137], v[178:181], v[98:101]
	s_nop 0
	v_mfma_i32_16x16x64_i8 v[98:101], v[130:133], v[182:185], v[98:101]
	v_mfma_i32_16x16x64_i8 v[114:117], v[158:161], v[186:189], v[114:117]
	s_nop 0
	v_mfma_i32_16x16x64_i8 v[114:117], v[154:157], v[190:193], v[114:117]
	v_mfma_i32_16x16x64_i8 v[122:125], v[150:153], v[186:189], v[122:125]
	s_nop 0
	v_mfma_i32_16x16x64_i8 v[122:125], v[146:149], v[190:193], v[122:125]
	v_mfma_i32_16x16x64_i8 v[118:121], v[142:145], v[186:189], v[118:121]
	s_nop 0
	v_mfma_i32_16x16x64_i8 v[118:121], v[138:141], v[190:193], v[118:121]
	v_mfma_i32_16x16x64_i8 v[126:129], v[134:137], v[186:189], v[126:129]
	s_nop 0
	v_mfma_i32_16x16x64_i8 v[126:129], v[130:133], v[190:193], v[126:129]
	s_setprio 0
	s_barrier
	v_mov_b32_e32 v205, v197
	s_add_i32 s43, s43, s10
	ds_read_b128 v[162:165], v204 offset:49152
	ds_read_b128 v[166:169], v204 offset:50176
	ds_read_b128 v[170:173], v204 offset:51200
	ds_read_b128 v[174:177], v204 offset:52224
	ds_read_b128 v[178:181], v204 offset:53248
	ds_read_b128 v[182:185], v204 offset:54272
	ds_read_b128 v[186:189], v204 offset:55296
	ds_read_b128 v[190:193], v204 offset:56320
	s_mov_b32 m0, s43
	s_nop 0
	global_load_lds_dwordx4 v205, s[50:51]
	v_mov_b32_e32 v205, v199
	s_add_i32 m0, s43, 0x2000
	s_nop 0
	global_load_lds_dwordx4 v205, s[50:51]
	s_add_u32 s50, s52, 0x40080
	s_addc_u32 s51, s53, 0
	v_mov_b32_e32 v205, v197
	s_add_i32 s43, s74, s10
	s_mov_b32 m0, s43
	s_nop 0
	global_load_lds_dwordx4 v205, s[50:51]
	v_mov_b32_e32 v205, v199
	s_add_i32 m0, s43, 0x2000
	s_nop 0
	global_load_lds_dwordx4 v205, s[50:51]
	s_waitcnt vmcnt(6)
	s_waitcnt lgkmcnt(0)
	s_barrier
	s_setprio 1
	s_waitcnt lgkmcnt(0)
	v_mfma_i32_16x16x64_i8 v[2:5], v[158:161], v[162:165], v[2:5]
	s_nop 0
	v_mfma_i32_16x16x64_i8 v[2:5], v[154:157], v[166:169], v[2:5]
	v_mfma_i32_16x16x64_i8 v[6:9], v[150:153], v[162:165], v[6:9]
	s_nop 0
	v_mfma_i32_16x16x64_i8 v[6:9], v[146:149], v[166:169], v[6:9]
	v_mfma_i32_16x16x64_i8 v[10:13], v[142:145], v[162:165], v[10:13]
	s_nop 0
	v_mfma_i32_16x16x64_i8 v[10:13], v[138:141], v[166:169], v[10:13]
	v_mfma_i32_16x16x64_i8 v[14:17], v[134:137], v[162:165], v[14:17]
	s_nop 0
	v_mfma_i32_16x16x64_i8 v[14:17], v[130:133], v[166:169], v[14:17]
	v_mfma_i32_16x16x64_i8 v[30:33], v[158:161], v[170:173], v[30:33]
	s_nop 0
	v_mfma_i32_16x16x64_i8 v[30:33], v[154:157], v[174:177], v[30:33]
	v_mfma_i32_16x16x64_i8 v[42:45], v[150:153], v[170:173], v[42:45]
	s_nop 0
	v_mfma_i32_16x16x64_i8 v[42:45], v[146:149], v[174:177], v[42:45]
	v_mfma_i32_16x16x64_i8 v[38:41], v[142:145], v[170:173], v[38:41]
	s_nop 0
	v_mfma_i32_16x16x64_i8 v[38:41], v[138:141], v[174:177], v[38:41]
	v_mfma_i32_16x16x64_i8 v[46:49], v[134:137], v[170:173], v[46:49]
	s_nop 0
	v_mfma_i32_16x16x64_i8 v[46:49], v[130:133], v[174:177], v[46:49]
	v_mfma_i32_16x16x64_i8 v[58:61], v[158:161], v[178:181], v[58:61]
	s_nop 0
	v_mfma_i32_16x16x64_i8 v[58:61], v[154:157], v[182:185], v[58:61]
	v_mfma_i32_16x16x64_i8 v[74:77], v[150:153], v[178:181], v[74:77]
	s_nop 0
	v_mfma_i32_16x16x64_i8 v[74:77], v[146:149], v[182:185], v[74:77]
	v_mfma_i32_16x16x64_i8 v[70:73], v[142:145], v[178:181], v[70:73]
	s_nop 0
	v_mfma_i32_16x16x64_i8 v[70:73], v[138:141], v[182:185], v[70:73]
	v_mfma_i32_16x16x64_i8 v[78:81], v[134:137], v[178:181], v[78:81]
	s_nop 0
	v_mfma_i32_16x16x64_i8 v[78:81], v[130:133], v[182:185], v[78:81]
	v_mfma_i32_16x16x64_i8 v[90:93], v[158:161], v[186:189], v[90:93]
	s_nop 0
	v_mfma_i32_16x16x64_i8 v[90:93], v[154:157], v[190:193], v[90:93]
	v_mfma_i32_16x16x64_i8 v[106:109], v[150:153], v[186:189], v[106:109]
	s_nop 0
	v_mfma_i32_16x16x64_i8 v[106:109], v[146:149], v[190:193], v[106:109]
	v_mfma_i32_16x16x64_i8 v[102:105], v[142:145], v[186:189], v[102:105]
	s_nop 0
	v_mfma_i32_16x16x64_i8 v[102:105], v[138:141], v[190:193], v[102:105]
	v_mfma_i32_16x16x64_i8 v[110:113], v[134:137], v[186:189], v[110:113]
	s_nop 0
	v_mfma_i32_16x16x64_i8 v[110:113], v[130:133], v[190:193], v[110:113]
	s_setprio 0
	s_barrier
	s_add_i32 s41, s41, 2
	s_add_u32 s48, s48, 0x100
	s_addc_u32 s49, s49, 0
	s_cmp_gt_u32 s41, 13
	s_cbranch_scc1 .LBB0_1098
	s_mov_b64 s[52:53], s[14:15]
	s_mov_b64 s[50:51], s[26:27]

.Li8b_1088_1084:
	s_waitcnt vmcnt(8)
	s_waitcnt lgkmcnt(0)
	s_barrier
	s_setprio 1
	v_mfma_i32_16x16x64_i8 v[18:21], v[158:161], v[190:193], v[18:21]
	s_nop 0
	v_mfma_i32_16x16x64_i8 v[18:21], v[154:157], v[186:189], v[18:21]
	v_mfma_i32_16x16x64_i8 v[22:25], v[150:153], v[190:193], v[22:25]
	s_nop 0
	v_mfma_i32_16x16x64_i8 v[22:25], v[142:145], v[186:189], v[22:25]
	v_mfma_i32_16x16x64_i8 v[26:29], v[146:149], v[190:193], v[26:29]
	s_nop 0
	v_mfma_i32_16x16x64_i8 v[26:29], v[138:141], v[186:189], v[26:29]
	v_mfma_i32_16x16x64_i8 v[34:37], v[134:137], v[190:193], v[34:37]
	s_nop 0
	v_mfma_i32_16x16x64_i8 v[34:37], v[130:133], v[186:189], v[34:37]
	v_mfma_i32_16x16x64_i8 v[50:53], v[158:161], v[182:185], v[50:53]
	s_nop 0
	v_mfma_i32_16x16x64_i8 v[50:53], v[154:157], v[178:181], v[50:53]
	v_mfma_i32_16x16x64_i8 v[62:65], v[150:153], v[182:185], v[62:65]
	s_nop 0
	v_mfma_i32_16x16x64_i8 v[62:65], v[142:145], v[178:181], v[62:65]
	v_mfma_i32_16x16x64_i8 v[54:57], v[146:149], v[182:185], v[54:57]
	s_nop 0
	v_mfma_i32_16x16x64_i8 v[54:57], v[138:141], v[178:181], v[54:57]
	v_mfma_i32_16x16x64_i8 v[66:69], v[134:137], v[182:185], v[66:69]
	s_nop 0
	v_mfma_i32_16x16x64_i8 v[66:69], v[130:133], v[178:181], v[66:69]
	v_mfma_i32_16x16x64_i8 v[82:85], v[158:161], v[174:177], v[82:85]
	s_nop 0
	v_mfma_i32_16x16x64_i8 v[82:85], v[154:157], v[170:173], v[82:85]
	v_mfma_i32_16x16x64_i8 v[94:97], v[150:153], v[174:177], v[94:97]
	s_nop 0
	v_mfma_i32_16x16x64_i8 v[94:97], v[142:145], v[170:173], v[94:97]
	v_mfma_i32_16x16x64_i8 v[86:89], v[146:149], v[174:177], v[86:89]
	s_nop 0
	v_mfma_i32_16x16x64_i8 v[86:89], v[138:141], v[170:173], v[86:89]
	v_mfma_i32_16x16x64_i8 v[98:101], v[134:137], v[174:177], v[98:101]
	s_nop 0
	v_mfma_i32_16x16x64_i8 v[98:101], v[130:133], v[170:173], v[98:101]
	v_mfma_i32_16x16x64_i8 v[114:117], v[158:161], v[166:169], v[114:117]
	s_nop 0
	v_mfma_i32_16x16x64_i8 v[114:117], v[154:157], v[162:165], v[114:117]
	v_mfma_i32_16x16x64_i8 v[122:125], v[150:153], v[166:169], v[122:125]
	s_nop 0
	v_mfma_i32_16x16x64_i8 v[122:125], v[142:145], v[162:165], v[122:125]
	v_mfma_i32_16x16x64_i8 v[118:121], v[146:149], v[166:169], v[118:121]
	s_nop 0
	v_mfma_i32_16x16x64_i8 v[118:121], v[138:141], v[162:165], v[118:121]
	v_mfma_i32_16x16x64_i8 v[126:129], v[134:137], v[166:169], v[126:129]
	s_nop 0
	v_mfma_i32_16x16x64_i8 v[126:129], v[130:133], v[162:165], v[126:129]
	s_setprio 0
	s_barrier
	s_add_u32 s81, s77, s48
	s_addc_u32 s82, s78, s49
	s_cmp_eq_u32 s41, 12
	s_cselect_b64 s[66:67], -1, 0
	s_and_b64 s[74:75], s[66:67], exec
	s_cselect_b32 s53, s53, s82
	s_cselect_b32 s52, s52, s81
	s_mov_b64 s[74:75], s[52:53]
	v_mov_b32_e32 v205, v197
	s_mov_b32 m0, s33
	s_waitcnt lgkmcnt(0)
	ds_read_b128 v[190:193], v204 offset:16384
	ds_read_b128 v[186:189], v204 offset:17408
	ds_read_b128 v[182:185], v204 offset:18432
	ds_read_b128 v[178:181], v204 offset:19456
	ds_read_b128 v[174:177], v204 offset:20480
	ds_read_b128 v[170:173], v204 offset:21504
	ds_read_b128 v[166:169], v204 offset:22528
	ds_read_b128 v[162:165], v204 offset:23552
	s_nop 0
	global_load_lds_dwordx4 v205, s[74:75]
	v_mov_b32_e32 v205, v199
	s_mov_b32 m0, s35
	s_nop 0
	global_load_lds_dwordx4 v205, s[74:75]
	s_add_u32 s74, s52, 0x40000
	s_addc_u32 s75, s53, 0
	v_mov_b32_e32 v205, v197
	s_mov_b32 m0, s60
	s_nop 0
	global_load_lds_dwordx4 v205, s[74:75]
	v_mov_b32_e32 v205, v199
	s_mov_b32 m0, s61
	s_nop 0
	global_load_lds_dwordx4 v205, s[74:75]
	s_waitcnt vmcnt(6)
	s_waitcnt lgkmcnt(0)
	s_barrier
	s_setprio 1
	v_mfma_i32_16x16x64_i8 v[2:5], v[158:161], v[190:193], v[2:5]
	s_nop 0
	v_mfma_i32_16x16x64_i8 v[2:5], v[154:157], v[186:189], v[2:5]
	v_mfma_i32_16x16x64_i8 v[6:9], v[150:153], v[190:193], v[6:9]
	s_nop 0
	v_mfma_i32_16x16x64_i8 v[6:9], v[142:145], v[186:189], v[6:9]
	v_mfma_i32_16x16x64_i8 v[10:13], v[146:149], v[190:193], v[10:13]
	s_nop 0
	v_mfma_i32_16x16x64_i8 v[10:13], v[138:141], v[186:189], v[10:13]
	v_mfma_i32_16x16x64_i8 v[14:17], v[134:137], v[190:193], v[14:17]
	s_nop 0
	v_mfma_i32_16x16x64_i8 v[14:17], v[130:133], v[186:189], v[14:17]
	v_mfma_i32_16x16x64_i8 v[30:33], v[158:161], v[182:185], v[30:33]
	s_nop 0
	v_mfma_i32_16x16x64_i8 v[30:33], v[154:157], v[178:181], v[30:33]
	v_mfma_i32_16x16x64_i8 v[42:45], v[150:153], v[182:185], v[42:45]
	s_nop 0
	v_mfma_i32_16x16x64_i8 v[42:45], v[142:145], v[178:181], v[42:45]
	v_mfma_i32_16x16x64_i8 v[38:41], v[146:149], v[182:185], v[38:41]
	s_nop 0
	v_mfma_i32_16x16x64_i8 v[38:41], v[138:141], v[178:181], v[38:41]
	v_mfma_i32_16x16x64_i8 v[46:49], v[134:137], v[182:185], v[46:49]
	s_nop 0
	v_mfma_i32_16x16x64_i8 v[46:49], v[130:133], v[178:181], v[46:49]
	v_mfma_i32_16x16x64_i8 v[58:61], v[158:161], v[174:177], v[58:61]
	s_nop 0
	v_mfma_i32_16x16x64_i8 v[58:61], v[154:157], v[170:173], v[58:61]
	v_mfma_i32_16x16x64_i8 v[74:77], v[150:153], v[174:177], v[74:77]
	s_nop 0
	v_mfma_i32_16x16x64_i8 v[74:77], v[142:145], v[170:173], v[74:77]
	v_mfma_i32_16x16x64_i8 v[70:73], v[146:149], v[174:177], v[70:73]
	s_nop 0
	v_mfma_i32_16x16x64_i8 v[70:73], v[138:141], v[170:173], v[70:73]
	v_mfma_i32_16x16x64_i8 v[78:81], v[134:137], v[174:177], v[78:81]
	s_nop 0
	v_mfma_i32_16x16x64_i8 v[78:81], v[130:133], v[170:173], v[78:81]
	v_mfma_i32_16x16x64_i8 v[90:93], v[158:161], v[166:169], v[90:93]
	s_nop 0
	v_mfma_i32_16x16x64_i8 v[90:93], v[154:157], v[162:165], v[90:93]
	v_mfma_i32_16x16x64_i8 v[106:109], v[150:153], v[166:169], v[106:109]
	s_nop 0
	v_mfma_i32_16x16x64_i8 v[106:109], v[142:145], v[162:165], v[106:109]
	v_mfma_i32_16x16x64_i8 v[102:105], v[146:149], v[166:169], v[102:105]
	s_nop 0
	v_mfma_i32_16x16x64_i8 v[102:105], v[138:141], v[162:165], v[102:105]
	v_mfma_i32_16x16x64_i8 v[110:113], v[134:137], v[166:169], v[110:113]
	s_nop 0
	v_mfma_i32_16x16x64_i8 v[110:113], v[130:133], v[162:165], v[110:113]
	s_setprio 0
	s_barrier
	s_add_u32 s43, s43, 0x100
	s_addc_u32 s74, s80, 0
	s_and_b64 s[64:65], s[66:67], exec
	s_cselect_b32 s65, s51, s74
	s_cselect_b32 s64, s50, s43
	s_add_u32 s50, s52, 0x80
	s_addc_u32 s51, s53, 0
	s_add_i32 s43, 0, 0x18000
	s_add_i32 s74, 0, 0x1c000
	v_add_u32_e32 v130, s43, v202
	v_add_u32_e32 v131, s74, v202
	ds_read_b128 v[158:161], v130
	ds_read_b128 v[154:157], v130 offset:1024
	ds_read_b128 v[150:153], v130 offset:2048
	ds_read_b128 v[146:149], v130 offset:3072
	ds_read_b128 v[142:145], v131
	ds_read_b128 v[138:141], v131 offset:1024
	ds_read_b128 v[134:137], v131 offset:2048
	ds_read_b128 v[130:133], v131 offset:3072
	s_mov_b64 s[66:67], s[64:65]
	v_mov_b32_e32 v205, v196
	s_mov_b32 m0, s5
	s_waitcnt lgkmcnt(0)
	ds_read_b128 v[162:165], v204 offset:32768
	ds_read_b128 v[166:169], v204 offset:33792
	ds_read_b128 v[170:173], v204 offset:34816
	ds_read_b128 v[174:177], v204 offset:35840
	ds_read_b128 v[178:181], v204 offset:36864
	ds_read_b128 v[182:185], v204 offset:37888
	ds_read_b128 v[186:189], v204 offset:38912
	ds_read_b128 v[190:193], v204 offset:39936
	s_add_u32 s64, s64, 0x40000
	global_load_lds_dwordx4 v205, s[66:67]
	v_mov_b32_e32 v205, v198
	s_mov_b32 m0, s62
	s_addc_u32 s65, s65, 0
	global_load_lds_dwordx4 v205, s[66:67]
	v_mov_b32_e32 v205, v196
	s_mov_b32 m0, s63
	s_nop 0
	global_load_lds_dwordx4 v205, s[64:65]
	v_mov_b32_e32 v205, v198
	s_mov_b32 m0, s69
	s_nop 0
	global_load_lds_dwordx4 v205, s[64:65]
	s_waitcnt vmcnt(8)
	s_waitcnt lgkmcnt(0)
	s_barrier
	s_setprio 1
	s_waitcnt lgkmcnt(0)
	v_mfma_i32_16x16x64_i8 v[18:21], v[158:161], v[162:165], v[18:21]
	s_nop 0
	v_mfma_i32_16x16x64_i8 v[18:21], v[154:157], v[166:169], v[18:21]
	v_mfma_i32_16x16x64_i8 v[22:25], v[150:153], v[162:165], v[22:25]
	s_nop 0
	v_mfma_i32_16x16x64_i8 v[22:25], v[146:149], v[166:169], v[22:25]
	v_mfma_i32_16x16x64_i8 v[26:29], v[142:145], v[162:165], v[26:29]
	s_nop 0
	v_mfma_i32_16x16x64_i8 v[26:29], v[138:141], v[166:169], v[26:29]
	v_mfma_i32_16x16x64_i8 v[34:37], v[134:137], v[162:165], v[34:37]
	s_nop 0
	v_mfma_i32_16x16x64_i8 v[34:37], v[130:133], v[166:169], v[34:37]
	v_mfma_i32_16x16x64_i8 v[50:53], v[158:161], v[170:173], v[50:53]
	s_nop 0
	v_mfma_i32_16x16x64_i8 v[50:53], v[154:157], v[174:177], v[50:53]
	v_mfma_i32_16x16x64_i8 v[62:65], v[150:153], v[170:173], v[62:65]
	s_nop 0
	v_mfma_i32_16x16x64_i8 v[62:65], v[146:149], v[174:177], v[62:65]
	v_mfma_i32_16x16x64_i8 v[54:57], v[142:145], v[170:173], v[54:57]
	s_nop 0
	v_mfma_i32_16x16x64_i8 v[54:57], v[138:141], v[174:177], v[54:57]
	v_mfma_i32_16x16x64_i8 v[66:69], v[134:137], v[170:173], v[66:69]
	s_nop 0
	v_mfma_i32_16x16x64_i8 v[66:69], v[130:133], v[174:177], v[66:69]
	v_mfma_i32_16x16x64_i8 v[82:85], v[158:161], v[178:181], v[82:85]
	s_nop 0
	v_mfma_i32_16x16x64_i8 v[82:85], v[154:157], v[182:185], v[82:85]
	v_mfma_i32_16x16x64_i8 v[94:97], v[150:153], v[178:181], v[94:97]
	s_nop 0
	v_mfma_i32_16x16x64_i8 v[94:97], v[146:149], v[182:185], v[94:97]
	v_mfma_i32_16x16x64_i8 v[86:89], v[142:145], v[178:181], v[86:89]
	s_nop 0
	v_mfma_i32_16x16x64_i8 v[86:89], v[138:141], v[182:185], v[86:89]
	v_mfma_i32_16x16x64_i8 v[98:101], v[134:137], v[178:181], v[98:101]
	s_nop 0
	v_mfma_i32_16x16x64_i8 v[98:101], v[130:133], v[182:185], v[98:101]
	v_mfma_i32_16x16x64_i8 v[114:117], v[158:161], v[186:189], v[114:117]
	s_nop 0
	v_mfma_i32_16x16x64_i8 v[114:117], v[154:157], v[190:193], v[114:117]
	v_mfma_i32_16x16x64_i8 v[122:125], v[150:153], v[186:189], v[122:125]
	s_nop 0
	v_mfma_i32_16x16x64_i8 v[122:125], v[146:149], v[190:193], v[122:125]
	v_mfma_i32_16x16x64_i8 v[118:121], v[142:145], v[186:189], v[118:121]
	s_nop 0
	v_mfma_i32_16x16x64_i8 v[118:121], v[138:141], v[190:193], v[118:121]
	v_mfma_i32_16x16x64_i8 v[126:129], v[134:137], v[186:189], v[126:129]
	s_nop 0
	v_mfma_i32_16x16x64_i8 v[126:129], v[130:133], v[190:193], v[126:129]
	s_setprio 0
	s_barrier
	v_mov_b32_e32 v205, v197
	s_add_i32 s43, s43, s10
	ds_read_b128 v[162:165], v204 offset:49152
	ds_read_b128 v[166:169], v204 offset:50176
	ds_read_b128 v[170:173], v204 offset:51200
	ds_read_b128 v[174:177], v204 offset:52224
	ds_read_b128 v[178:181], v204 offset:53248
	ds_read_b128 v[182:185], v204 offset:54272
	ds_read_b128 v[186:189], v204 offset:55296
	ds_read_b128 v[190:193], v204 offset:56320
	s_mov_b32 m0, s43
	s_nop 0
	global_load_lds_dwordx4 v205, s[50:51]
	v_mov_b32_e32 v205, v199
	s_add_i32 m0, s43, 0x2000
	s_nop 0
	global_load_lds_dwordx4 v205, s[50:51]
	s_add_u32 s50, s52, 0x40080
	s_addc_u32 s51, s53, 0
	v_mov_b32_e32 v205, v197
	s_add_i32 s43, s74, s10
	s_mov_b32 m0, s43
	s_nop 0
	global_load_lds_dwordx4 v205, s[50:51]
	v_mov_b32_e32 v205, v199
	s_add_i32 m0, s43, 0x2000
	s_nop 0
	global_load_lds_dwordx4 v205, s[50:51]
	s_waitcnt vmcnt(6)
	s_waitcnt lgkmcnt(0)
	s_barrier
	s_setprio 1
	s_waitcnt lgkmcnt(0)
	v_mfma_i32_16x16x64_i8 v[2:5], v[158:161], v[162:165], v[2:5]
	s_nop 0
	v_mfma_i32_16x16x64_i8 v[2:5], v[154:157], v[166:169], v[2:5]
	v_mfma_i32_16x16x64_i8 v[6:9], v[150:153], v[162:165], v[6:9]
	s_nop 0
	v_mfma_i32_16x16x64_i8 v[6:9], v[146:149], v[166:169], v[6:9]
	v_mfma_i32_16x16x64_i8 v[10:13], v[142:145], v[162:165], v[10:13]
	s_nop 0
	v_mfma_i32_16x16x64_i8 v[10:13], v[138:141], v[166:169], v[10:13]
	v_mfma_i32_16x16x64_i8 v[14:17], v[134:137], v[162:165], v[14:17]
	s_nop 0
	v_mfma_i32_16x16x64_i8 v[14:17], v[130:133], v[166:169], v[14:17]
	v_mfma_i32_16x16x64_i8 v[30:33], v[158:161], v[170:173], v[30:33]
	s_nop 0
	v_mfma_i32_16x16x64_i8 v[30:33], v[154:157], v[174:177], v[30:33]
	v_mfma_i32_16x16x64_i8 v[42:45], v[150:153], v[170:173], v[42:45]
	s_nop 0
	v_mfma_i32_16x16x64_i8 v[42:45], v[146:149], v[174:177], v[42:45]
	v_mfma_i32_16x16x64_i8 v[38:41], v[142:145], v[170:173], v[38:41]
	s_nop 0
	v_mfma_i32_16x16x64_i8 v[38:41], v[138:141], v[174:177], v[38:41]
	v_mfma_i32_16x16x64_i8 v[46:49], v[134:137], v[170:173], v[46:49]
	s_nop 0
	v_mfma_i32_16x16x64_i8 v[46:49], v[130:133], v[174:177], v[46:49]
	v_mfma_i32_16x16x64_i8 v[58:61], v[158:161], v[178:181], v[58:61]
	s_nop 0
	v_mfma_i32_16x16x64_i8 v[58:61], v[154:157], v[182:185], v[58:61]
	v_mfma_i32_16x16x64_i8 v[74:77], v[150:153], v[178:181], v[74:77]
	s_nop 0
	v_mfma_i32_16x16x64_i8 v[74:77], v[146:149], v[182:185], v[74:77]
	v_mfma_i32_16x16x64_i8 v[70:73], v[142:145], v[178:181], v[70:73]
	s_nop 0
	v_mfma_i32_16x16x64_i8 v[70:73], v[138:141], v[182:185], v[70:73]
	v_mfma_i32_16x16x64_i8 v[78:81], v[134:137], v[178:181], v[78:81]
	s_nop 0
	v_mfma_i32_16x16x64_i8 v[78:81], v[130:133], v[182:185], v[78:81]
	v_mfma_i32_16x16x64_i8 v[90:93], v[158:161], v[186:189], v[90:93]
	s_nop 0
	v_mfma_i32_16x16x64_i8 v[90:93], v[154:157], v[190:193], v[90:93]
	v_mfma_i32_16x16x64_i8 v[106:109], v[150:153], v[186:189], v[106:109]
	s_nop 0
	v_mfma_i32_16x16x64_i8 v[106:109], v[146:149], v[190:193], v[106:109]
	v_mfma_i32_16x16x64_i8 v[102:105], v[142:145], v[186:189], v[102:105]
	s_nop 0
	v_mfma_i32_16x16x64_i8 v[102:105], v[138:141], v[190:193], v[102:105]
	v_mfma_i32_16x16x64_i8 v[110:113], v[134:137], v[186:189], v[110:113]
	s_nop 0
	v_mfma_i32_16x16x64_i8 v[110:113], v[130:133], v[190:193], v[110:113]
	s_setprio 0
	s_barrier
	s_add_i32 s41, s41, 2
	s_add_u32 s48, s48, 0x100
	s_addc_u32 s49, s49, 0
	s_cmp_gt_u32 s41, 13
	s_cbranch_scc1 .LBB0_1098
	s_mov_b64 s[52:53], s[14:15]
	s_mov_b64 s[50:51], s[26:27]
	s_branch .Li8loop_1084

.LBB0_1298:
	s_waitcnt vmcnt(8)
	s_waitcnt lgkmcnt(0)
	s_barrier
	s_setprio 1
	v_mfma_i32_16x16x64_i8 v[18:21], v[158:161], v[190:193], 0
	s_nop 0
	v_mfma_i32_16x16x64_i8 v[18:21], v[154:157], v[186:189], v[18:21]
	v_mfma_i32_16x16x64_i8 v[22:25], v[150:153], v[190:193], 0
	s_nop 0
	v_mfma_i32_16x16x64_i8 v[22:25], v[142:145], v[186:189], v[22:25]
	v_mfma_i32_16x16x64_i8 v[26:29], v[146:149], v[190:193], 0
	s_nop 0
	v_mfma_i32_16x16x64_i8 v[26:29], v[138:141], v[186:189], v[26:29]
	v_mfma_i32_16x16x64_i8 v[34:37], v[134:137], v[190:193], 0
	s_nop 0
	v_mfma_i32_16x16x64_i8 v[34:37], v[130:133], v[186:189], v[34:37]
	v_mfma_i32_16x16x64_i8 v[50:53], v[158:161], v[182:185], 0
	s_nop 0
	v_mfma_i32_16x16x64_i8 v[50:53], v[154:157], v[178:181], v[50:53]
	v_mfma_i32_16x16x64_i8 v[62:65], v[150:153], v[182:185], 0
	s_nop 0
	v_mfma_i32_16x16x64_i8 v[62:65], v[142:145], v[178:181], v[62:65]
	v_mfma_i32_16x16x64_i8 v[54:57], v[146:149], v[182:185], 0
	s_nop 0
	v_mfma_i32_16x16x64_i8 v[54:57], v[138:141], v[178:181], v[54:57]
	v_mfma_i32_16x16x64_i8 v[66:69], v[134:137], v[182:185], 0
	s_nop 0
	v_mfma_i32_16x16x64_i8 v[66:69], v[130:133], v[178:181], v[66:69]
	v_mfma_i32_16x16x64_i8 v[82:85], v[158:161], v[174:177], 0
	s_nop 0
	v_mfma_i32_16x16x64_i8 v[82:85], v[154:157], v[170:173], v[82:85]
	v_mfma_i32_16x16x64_i8 v[94:97], v[150:153], v[174:177], 0
	s_nop 0
	v_mfma_i32_16x16x64_i8 v[94:97], v[142:145], v[170:173], v[94:97]
	v_mfma_i32_16x16x64_i8 v[86:89], v[146:149], v[174:177], 0
	s_nop 0
	v_mfma_i32_16x16x64_i8 v[86:89], v[138:141], v[170:173], v[86:89]
	v_mfma_i32_16x16x64_i8 v[98:101], v[134:137], v[174:177], 0
	s_nop 0
	v_mfma_i32_16x16x64_i8 v[98:101], v[130:133], v[170:173], v[98:101]
	v_mfma_i32_16x16x64_i8 v[114:117], v[158:161], v[166:169], 0
	s_nop 0
	v_mfma_i32_16x16x64_i8 v[114:117], v[154:157], v[162:165], v[114:117]
	v_mfma_i32_16x16x64_i8 v[122:125], v[150:153], v[166:169], 0
	s_nop 0
	v_mfma_i32_16x16x64_i8 v[122:125], v[142:145], v[162:165], v[122:125]
	v_mfma_i32_16x16x64_i8 v[118:121], v[146:149], v[166:169], 0
	s_nop 0
	v_mfma_i32_16x16x64_i8 v[118:121], v[138:141], v[162:165], v[118:121]
	v_mfma_i32_16x16x64_i8 v[126:129], v[134:137], v[166:169], 0
	s_nop 0
	v_mfma_i32_16x16x64_i8 v[126:129], v[130:133], v[162:165], v[126:129]
	s_setprio 0
	s_barrier
	s_add_u32 s81, s77, s48
	s_addc_u32 s82, s78, s49
	s_cmp_eq_u32 s41, 12
	s_cselect_b64 s[66:67], -1, 0
	s_and_b64 s[74:75], s[66:67], exec
	s_cselect_b32 s53, s53, s82
	s_cselect_b32 s52, s52, s81
	s_mov_b64 s[74:75], s[52:53]
	v_mov_b32_e32 v203, v196
	s_mov_b32 m0, s33
	s_waitcnt lgkmcnt(0)
	ds_read_b128 v[190:193], v202 offset:16384
	ds_read_b128 v[186:189], v202 offset:17408
	ds_read_b128 v[182:185], v202 offset:18432
	ds_read_b128 v[178:181], v202 offset:19456
	ds_read_b128 v[174:177], v202 offset:20480
	ds_read_b128 v[170:173], v202 offset:21504
	ds_read_b128 v[166:169], v202 offset:22528
	ds_read_b128 v[162:165], v202 offset:23552
	s_nop 0
	global_load_lds_dwordx4 v203, s[74:75]
	v_mov_b32_e32 v203, v197
	s_mov_b32 m0, s35
	s_nop 0
	global_load_lds_dwordx4 v203, s[74:75]
	s_add_u32 s74, s52, 0x40000
	s_addc_u32 s75, s53, 0
	v_mov_b32_e32 v203, v196
	s_mov_b32 m0, s60
	s_nop 0
	global_load_lds_dwordx4 v203, s[74:75]
	v_mov_b32_e32 v203, v197
	s_mov_b32 m0, s61
	s_nop 0
	global_load_lds_dwordx4 v203, s[74:75]
	s_waitcnt vmcnt(6)
	s_waitcnt lgkmcnt(0)
	s_barrier
	s_setprio 1
	v_mfma_i32_16x16x64_i8 v[2:5], v[158:161], v[190:193], 0
	s_nop 0
	v_mfma_i32_16x16x64_i8 v[2:5], v[154:157], v[186:189], v[2:5]
	v_mfma_i32_16x16x64_i8 v[6:9], v[150:153], v[190:193], 0
	s_nop 0
	v_mfma_i32_16x16x64_i8 v[6:9], v[142:145], v[186:189], v[6:9]
	v_mfma_i32_16x16x64_i8 v[10:13], v[146:149], v[190:193], 0
	s_nop 0
	v_mfma_i32_16x16x64_i8 v[10:13], v[138:141], v[186:189], v[10:13]
	v_mfma_i32_16x16x64_i8 v[14:17], v[134:137], v[190:193], 0
	s_nop 0
	v_mfma_i32_16x16x64_i8 v[14:17], v[130:133], v[186:189], v[14:17]
	v_mfma_i32_16x16x64_i8 v[30:33], v[158:161], v[182:185], 0
	s_nop 0
	v_mfma_i32_16x16x64_i8 v[30:33], v[154:157], v[178:181], v[30:33]
	v_mfma_i32_16x16x64_i8 v[42:45], v[150:153], v[182:185], 0
	s_nop 0
	v_mfma_i32_16x16x64_i8 v[42:45], v[142:145], v[178:181], v[42:45]
	v_mfma_i32_16x16x64_i8 v[38:41], v[146:149], v[182:185], 0
	s_nop 0
	v_mfma_i32_16x16x64_i8 v[38:41], v[138:141], v[178:181], v[38:41]
	v_mfma_i32_16x16x64_i8 v[46:49], v[134:137], v[182:185], 0
	s_nop 0
	v_mfma_i32_16x16x64_i8 v[46:49], v[130:133], v[178:181], v[46:49]
	v_mfma_i32_16x16x64_i8 v[58:61], v[158:161], v[174:177], 0
	s_nop 0
	v_mfma_i32_16x16x64_i8 v[58:61], v[154:157], v[170:173], v[58:61]
	v_mfma_i32_16x16x64_i8 v[74:77], v[150:153], v[174:177], 0
	s_nop 0
	v_mfma_i32_16x16x64_i8 v[74:77], v[142:145], v[170:173], v[74:77]
	v_mfma_i32_16x16x64_i8 v[70:73], v[146:149], v[174:177], 0
	s_nop 0
	v_mfma_i32_16x16x64_i8 v[70:73], v[138:141], v[170:173], v[70:73]
	v_mfma_i32_16x16x64_i8 v[78:81], v[134:137], v[174:177], 0
	s_nop 0
	v_mfma_i32_16x16x64_i8 v[78:81], v[130:133], v[170:173], v[78:81]
	v_mfma_i32_16x16x64_i8 v[90:93], v[158:161], v[166:169], 0
	s_nop 0
	v_mfma_i32_16x16x64_i8 v[90:93], v[154:157], v[162:165], v[90:93]
	v_mfma_i32_16x16x64_i8 v[106:109], v[150:153], v[166:169], 0
	s_nop 0
	v_mfma_i32_16x16x64_i8 v[106:109], v[142:145], v[162:165], v[106:109]
	v_mfma_i32_16x16x64_i8 v[102:105], v[146:149], v[166:169], 0
	s_nop 0
	v_mfma_i32_16x16x64_i8 v[102:105], v[138:141], v[162:165], v[102:105]
	v_mfma_i32_16x16x64_i8 v[110:113], v[134:137], v[166:169], 0
	s_nop 0
	v_mfma_i32_16x16x64_i8 v[110:113], v[130:133], v[162:165], v[110:113]
	s_setprio 0
	s_barrier
	s_add_u32 s43, s43, 0x100
	s_addc_u32 s74, s80, 0
	s_and_b64 s[64:65], s[66:67], exec
	s_cselect_b32 s65, s51, s74
	s_cselect_b32 s64, s50, s43
	s_add_u32 s50, s52, 0x80
	s_addc_u32 s51, s53, 0
	s_add_i32 s43, 0, 0x18000
	s_add_i32 s74, 0, 0x1c000
	v_add_u32_e32 v130, s43, v199
	v_add_u32_e32 v131, s74, v199
	ds_read_b128 v[158:161], v130
	ds_read_b128 v[154:157], v130 offset:1024
	ds_read_b128 v[150:153], v130 offset:2048
	ds_read_b128 v[146:149], v130 offset:3072
	ds_read_b128 v[142:145], v131
	ds_read_b128 v[138:141], v131 offset:1024
	ds_read_b128 v[134:137], v131 offset:2048
	ds_read_b128 v[130:133], v131 offset:3072
	s_mov_b64 s[66:67], s[64:65]
	v_mov_b32_e32 v203, v196
	s_mov_b32 m0, s5
	s_waitcnt lgkmcnt(0)
	ds_read_b128 v[162:165], v202 offset:32768
	ds_read_b128 v[166:169], v202 offset:33792
	ds_read_b128 v[170:173], v202 offset:34816
	ds_read_b128 v[174:177], v202 offset:35840
	ds_read_b128 v[178:181], v202 offset:36864
	ds_read_b128 v[182:185], v202 offset:37888
	ds_read_b128 v[186:189], v202 offset:38912
	ds_read_b128 v[190:193], v202 offset:39936
	s_add_u32 s64, s64, 0x40000
	global_load_lds_dwordx4 v203, s[66:67]
	v_mov_b32_e32 v203, v197
	s_mov_b32 m0, s62
	s_addc_u32 s65, s65, 0
	global_load_lds_dwordx4 v203, s[66:67]
	v_mov_b32_e32 v203, v196
	s_mov_b32 m0, s63
	s_nop 0
	global_load_lds_dwordx4 v203, s[64:65]
	v_mov_b32_e32 v203, v197
	s_mov_b32 m0, s69
	s_nop 0
	global_load_lds_dwordx4 v203, s[64:65]
	s_waitcnt vmcnt(8)
	s_waitcnt lgkmcnt(0)
	s_barrier
	s_setprio 1
	s_waitcnt lgkmcnt(0)
	v_mfma_i32_16x16x64_i8 v[18:21], v[158:161], v[162:165], v[18:21]
	s_nop 0
	v_mfma_i32_16x16x64_i8 v[18:21], v[154:157], v[166:169], v[18:21]
	v_mfma_i32_16x16x64_i8 v[22:25], v[150:153], v[162:165], v[22:25]
	s_nop 0
	v_mfma_i32_16x16x64_i8 v[22:25], v[146:149], v[166:169], v[22:25]
	v_mfma_i32_16x16x64_i8 v[26:29], v[142:145], v[162:165], v[26:29]
	s_nop 0
	v_mfma_i32_16x16x64_i8 v[26:29], v[138:141], v[166:169], v[26:29]
	v_mfma_i32_16x16x64_i8 v[34:37], v[134:137], v[162:165], v[34:37]
	s_nop 0
	v_mfma_i32_16x16x64_i8 v[34:37], v[130:133], v[166:169], v[34:37]
	v_mfma_i32_16x16x64_i8 v[50:53], v[158:161], v[170:173], v[50:53]
	s_nop 0
	v_mfma_i32_16x16x64_i8 v[50:53], v[154:157], v[174:177], v[50:53]
	v_mfma_i32_16x16x64_i8 v[62:65], v[150:153], v[170:173], v[62:65]
	s_nop 0
	v_mfma_i32_16x16x64_i8 v[62:65], v[146:149], v[174:177], v[62:65]
	v_mfma_i32_16x16x64_i8 v[54:57], v[142:145], v[170:173], v[54:57]
	s_nop 0
	v_mfma_i32_16x16x64_i8 v[54:57], v[138:141], v[174:177], v[54:57]
	v_mfma_i32_16x16x64_i8 v[66:69], v[134:137], v[170:173], v[66:69]
	s_nop 0
	v_mfma_i32_16x16x64_i8 v[66:69], v[130:133], v[174:177], v[66:69]
	v_mfma_i32_16x16x64_i8 v[82:85], v[158:161], v[178:181], v[82:85]
	s_nop 0
	v_mfma_i32_16x16x64_i8 v[82:85], v[154:157], v[182:185], v[82:85]
	v_mfma_i32_16x16x64_i8 v[94:97], v[150:153], v[178:181], v[94:97]
	s_nop 0
	v_mfma_i32_16x16x64_i8 v[94:97], v[146:149], v[182:185], v[94:97]
	v_mfma_i32_16x16x64_i8 v[86:89], v[142:145], v[178:181], v[86:89]
	s_nop 0
	v_mfma_i32_16x16x64_i8 v[86:89], v[138:141], v[182:185], v[86:89]
	v_mfma_i32_16x16x64_i8 v[98:101], v[134:137], v[178:181], v[98:101]
	s_nop 0
	v_mfma_i32_16x16x64_i8 v[98:101], v[130:133], v[182:185], v[98:101]
	v_mfma_i32_16x16x64_i8 v[114:117], v[158:161], v[186:189], v[114:117]
	s_nop 0
	v_mfma_i32_16x16x64_i8 v[114:117], v[154:157], v[190:193], v[114:117]
	v_mfma_i32_16x16x64_i8 v[122:125], v[150:153], v[186:189], v[122:125]
	s_nop 0
	v_mfma_i32_16x16x64_i8 v[122:125], v[146:149], v[190:193], v[122:125]
	v_mfma_i32_16x16x64_i8 v[118:121], v[142:145], v[186:189], v[118:121]
	s_nop 0
	v_mfma_i32_16x16x64_i8 v[118:121], v[138:141], v[190:193], v[118:121]
	v_mfma_i32_16x16x64_i8 v[126:129], v[134:137], v[186:189], v[126:129]
	s_nop 0
	v_mfma_i32_16x16x64_i8 v[126:129], v[130:133], v[190:193], v[126:129]
	s_setprio 0
	s_barrier
	v_mov_b32_e32 v203, v196
	s_add_i32 s43, s43, s10
	ds_read_b128 v[162:165], v202 offset:49152
	ds_read_b128 v[166:169], v202 offset:50176
	ds_read_b128 v[170:173], v202 offset:51200
	ds_read_b128 v[174:177], v202 offset:52224
	ds_read_b128 v[178:181], v202 offset:53248
	ds_read_b128 v[182:185], v202 offset:54272
	ds_read_b128 v[186:189], v202 offset:55296
	ds_read_b128 v[190:193], v202 offset:56320
	s_mov_b32 m0, s43
	s_nop 0
	global_load_lds_dwordx4 v203, s[50:51]
	v_mov_b32_e32 v203, v197
	s_add_i32 m0, s43, 0x2000
	s_nop 0
	global_load_lds_dwordx4 v203, s[50:51]
	s_add_u32 s50, s52, 0x40080
	s_addc_u32 s51, s53, 0
	v_mov_b32_e32 v203, v196
	s_add_i32 s43, s74, s10
	s_mov_b32 m0, s43
	s_nop 0
	global_load_lds_dwordx4 v203, s[50:51]
	v_mov_b32_e32 v203, v197
	s_add_i32 m0, s43, 0x2000
	s_nop 0
	global_load_lds_dwordx4 v203, s[50:51]
	s_waitcnt vmcnt(6)
	s_waitcnt lgkmcnt(0)
	s_barrier
	s_setprio 1
	s_waitcnt lgkmcnt(0)
	v_mfma_i32_16x16x64_i8 v[2:5], v[158:161], v[162:165], v[2:5]
	s_nop 0
	v_mfma_i32_16x16x64_i8 v[2:5], v[154:157], v[166:169], v[2:5]
	v_mfma_i32_16x16x64_i8 v[6:9], v[150:153], v[162:165], v[6:9]
	s_nop 0
	v_mfma_i32_16x16x64_i8 v[6:9], v[146:149], v[166:169], v[6:9]
	v_mfma_i32_16x16x64_i8 v[10:13], v[142:145], v[162:165], v[10:13]
	s_nop 0
	v_mfma_i32_16x16x64_i8 v[10:13], v[138:141], v[166:169], v[10:13]
	v_mfma_i32_16x16x64_i8 v[14:17], v[134:137], v[162:165], v[14:17]
	s_nop 0
	v_mfma_i32_16x16x64_i8 v[14:17], v[130:133], v[166:169], v[14:17]
	v_mfma_i32_16x16x64_i8 v[30:33], v[158:161], v[170:173], v[30:33]
	s_nop 0
	v_mfma_i32_16x16x64_i8 v[30:33], v[154:157], v[174:177], v[30:33]
	v_mfma_i32_16x16x64_i8 v[42:45], v[150:153], v[170:173], v[42:45]
	s_nop 0
	v_mfma_i32_16x16x64_i8 v[42:45], v[146:149], v[174:177], v[42:45]
	v_mfma_i32_16x16x64_i8 v[38:41], v[142:145], v[170:173], v[38:41]
	s_nop 0
	v_mfma_i32_16x16x64_i8 v[38:41], v[138:141], v[174:177], v[38:41]
	v_mfma_i32_16x16x64_i8 v[46:49], v[134:137], v[170:173], v[46:49]
	s_nop 0
	v_mfma_i32_16x16x64_i8 v[46:49], v[130:133], v[174:177], v[46:49]
	v_mfma_i32_16x16x64_i8 v[58:61], v[158:161], v[178:181], v[58:61]
	s_nop 0
	v_mfma_i32_16x16x64_i8 v[58:61], v[154:157], v[182:185], v[58:61]
	v_mfma_i32_16x16x64_i8 v[74:77], v[150:153], v[178:181], v[74:77]
	s_nop 0
	v_mfma_i32_16x16x64_i8 v[74:77], v[146:149], v[182:185], v[74:77]
	v_mfma_i32_16x16x64_i8 v[70:73], v[142:145], v[178:181], v[70:73]
	s_nop 0
	v_mfma_i32_16x16x64_i8 v[70:73], v[138:141], v[182:185], v[70:73]
	v_mfma_i32_16x16x64_i8 v[78:81], v[134:137], v[178:181], v[78:81]
	s_nop 0
	v_mfma_i32_16x16x64_i8 v[78:81], v[130:133], v[182:185], v[78:81]
	v_mfma_i32_16x16x64_i8 v[90:93], v[158:161], v[186:189], v[90:93]
	s_nop 0
	v_mfma_i32_16x16x64_i8 v[90:93], v[154:157], v[190:193], v[90:93]
	v_mfma_i32_16x16x64_i8 v[106:109], v[150:153], v[186:189], v[106:109]
	s_nop 0
	v_mfma_i32_16x16x64_i8 v[106:109], v[146:149], v[190:193], v[106:109]
	v_mfma_i32_16x16x64_i8 v[102:105], v[142:145], v[186:189], v[102:105]
	s_nop 0
	v_mfma_i32_16x16x64_i8 v[102:105], v[138:141], v[190:193], v[102:105]
	v_mfma_i32_16x16x64_i8 v[110:113], v[134:137], v[186:189], v[110:113]
	s_nop 0
	v_mfma_i32_16x16x64_i8 v[110:113], v[130:133], v[190:193], v[110:113]
	s_setprio 0
	s_barrier
	s_add_i32 s41, s41, 2
	s_add_u32 s48, s48, 0x100
	s_addc_u32 s49, s49, 0
	s_cmp_gt_u32 s41, 13
	s_cbranch_scc1 .LBB0_1308
	s_mov_b64 s[52:53], s[14:15]
	s_mov_b64 s[50:51], s[18:19]

.Li8b_1298_1294:
	s_waitcnt vmcnt(8)
	s_waitcnt lgkmcnt(0)
	s_barrier
	s_setprio 1
	v_mfma_i32_16x16x64_i8 v[18:21], v[158:161], v[190:193], v[18:21]
	s_nop 0
	v_mfma_i32_16x16x64_i8 v[18:21], v[154:157], v[186:189], v[18:21]
	v_mfma_i32_16x16x64_i8 v[22:25], v[150:153], v[190:193], v[22:25]
	s_nop 0
	v_mfma_i32_16x16x64_i8 v[22:25], v[142:145], v[186:189], v[22:25]
	v_mfma_i32_16x16x64_i8 v[26:29], v[146:149], v[190:193], v[26:29]
	s_nop 0
	v_mfma_i32_16x16x64_i8 v[26:29], v[138:141], v[186:189], v[26:29]
	v_mfma_i32_16x16x64_i8 v[34:37], v[134:137], v[190:193], v[34:37]
	s_nop 0
	v_mfma_i32_16x16x64_i8 v[34:37], v[130:133], v[186:189], v[34:37]
	v_mfma_i32_16x16x64_i8 v[50:53], v[158:161], v[182:185], v[50:53]
	s_nop 0
	v_mfma_i32_16x16x64_i8 v[50:53], v[154:157], v[178:181], v[50:53]
	v_mfma_i32_16x16x64_i8 v[62:65], v[150:153], v[182:185], v[62:65]
	s_nop 0
	v_mfma_i32_16x16x64_i8 v[62:65], v[142:145], v[178:181], v[62:65]
	v_mfma_i32_16x16x64_i8 v[54:57], v[146:149], v[182:185], v[54:57]
	s_nop 0
	v_mfma_i32_16x16x64_i8 v[54:57], v[138:141], v[178:181], v[54:57]
	v_mfma_i32_16x16x64_i8 v[66:69], v[134:137], v[182:185], v[66:69]
	s_nop 0
	v_mfma_i32_16x16x64_i8 v[66:69], v[130:133], v[178:181], v[66:69]
	v_mfma_i32_16x16x64_i8 v[82:85], v[158:161], v[174:177], v[82:85]
	s_nop 0
	v_mfma_i32_16x16x64_i8 v[82:85], v[154:157], v[170:173], v[82:85]
	v_mfma_i32_16x16x64_i8 v[94:97], v[150:153], v[174:177], v[94:97]
	s_nop 0
	v_mfma_i32_16x16x64_i8 v[94:97], v[142:145], v[170:173], v[94:97]
	v_mfma_i32_16x16x64_i8 v[86:89], v[146:149], v[174:177], v[86:89]
	s_nop 0
	v_mfma_i32_16x16x64_i8 v[86:89], v[138:141], v[170:173], v[86:89]
	v_mfma_i32_16x16x64_i8 v[98:101], v[134:137], v[174:177], v[98:101]
	s_nop 0
	v_mfma_i32_16x16x64_i8 v[98:101], v[130:133], v[170:173], v[98:101]
	v_mfma_i32_16x16x64_i8 v[114:117], v[158:161], v[166:169], v[114:117]
	s_nop 0
	v_mfma_i32_16x16x64_i8 v[114:117], v[154:157], v[162:165], v[114:117]
	v_mfma_i32_16x16x64_i8 v[122:125], v[150:153], v[166:169], v[122:125]
	s_nop 0
	v_mfma_i32_16x16x64_i8 v[122:125], v[142:145], v[162:165], v[122:125]
	v_mfma_i32_16x16x64_i8 v[118:121], v[146:149], v[166:169], v[118:121]
	s_nop 0
	v_mfma_i32_16x16x64_i8 v[118:121], v[138:141], v[162:165], v[118:121]
	v_mfma_i32_16x16x64_i8 v[126:129], v[134:137], v[166:169], v[126:129]
	s_nop 0
	v_mfma_i32_16x16x64_i8 v[126:129], v[130:133], v[162:165], v[126:129]
	s_setprio 0
	s_barrier
	s_add_u32 s81, s77, s48
	s_addc_u32 s82, s78, s49
	s_cmp_eq_u32 s41, 12
	s_cselect_b64 s[66:67], -1, 0
	s_and_b64 s[74:75], s[66:67], exec
	s_cselect_b32 s53, s53, s82
	s_cselect_b32 s52, s52, s81
	s_mov_b64 s[74:75], s[52:53]
	v_mov_b32_e32 v203, v196
	s_mov_b32 m0, s33
	s_waitcnt lgkmcnt(0)
	ds_read_b128 v[190:193], v202 offset:16384
	ds_read_b128 v[186:189], v202 offset:17408
	ds_read_b128 v[182:185], v202 offset:18432
	ds_read_b128 v[178:181], v202 offset:19456
	ds_read_b128 v[174:177], v202 offset:20480
	ds_read_b128 v[170:173], v202 offset:21504
	ds_read_b128 v[166:169], v202 offset:22528
	ds_read_b128 v[162:165], v202 offset:23552
	s_nop 0
	global_load_lds_dwordx4 v203, s[74:75]
	v_mov_b32_e32 v203, v197
	s_mov_b32 m0, s35
	s_nop 0
	global_load_lds_dwordx4 v203, s[74:75]
	s_add_u32 s74, s52, 0x40000
	s_addc_u32 s75, s53, 0
	v_mov_b32_e32 v203, v196
	s_mov_b32 m0, s60
	s_nop 0
	global_load_lds_dwordx4 v203, s[74:75]
	v_mov_b32_e32 v203, v197
	s_mov_b32 m0, s61
	s_nop 0
	global_load_lds_dwordx4 v203, s[74:75]
	s_waitcnt vmcnt(6)
	s_waitcnt lgkmcnt(0)
	s_barrier
	s_setprio 1
	v_mfma_i32_16x16x64_i8 v[2:5], v[158:161], v[190:193], v[2:5]
	s_nop 0
	v_mfma_i32_16x16x64_i8 v[2:5], v[154:157], v[186:189], v[2:5]
	v_mfma_i32_16x16x64_i8 v[6:9], v[150:153], v[190:193], v[6:9]
	s_nop 0
	v_mfma_i32_16x16x64_i8 v[6:9], v[142:145], v[186:189], v[6:9]
	v_mfma_i32_16x16x64_i8 v[10:13], v[146:149], v[190:193], v[10:13]
	s_nop 0
	v_mfma_i32_16x16x64_i8 v[10:13], v[138:141], v[186:189], v[10:13]
	v_mfma_i32_16x16x64_i8 v[14:17], v[134:137], v[190:193], v[14:17]
	s_nop 0
	v_mfma_i32_16x16x64_i8 v[14:17], v[130:133], v[186:189], v[14:17]
	v_mfma_i32_16x16x64_i8 v[30:33], v[158:161], v[182:185], v[30:33]
	s_nop 0
	v_mfma_i32_16x16x64_i8 v[30:33], v[154:157], v[178:181], v[30:33]
	v_mfma_i32_16x16x64_i8 v[42:45], v[150:153], v[182:185], v[42:45]
	s_nop 0
	v_mfma_i32_16x16x64_i8 v[42:45], v[142:145], v[178:181], v[42:45]
	v_mfma_i32_16x16x64_i8 v[38:41], v[146:149], v[182:185], v[38:41]
	s_nop 0
	v_mfma_i32_16x16x64_i8 v[38:41], v[138:141], v[178:181], v[38:41]
	v_mfma_i32_16x16x64_i8 v[46:49], v[134:137], v[182:185], v[46:49]
	s_nop 0
	v_mfma_i32_16x16x64_i8 v[46:49], v[130:133], v[178:181], v[46:49]
	v_mfma_i32_16x16x64_i8 v[58:61], v[158:161], v[174:177], v[58:61]
	s_nop 0
	v_mfma_i32_16x16x64_i8 v[58:61], v[154:157], v[170:173], v[58:61]
	v_mfma_i32_16x16x64_i8 v[74:77], v[150:153], v[174:177], v[74:77]
	s_nop 0
	v_mfma_i32_16x16x64_i8 v[74:77], v[142:145], v[170:173], v[74:77]
	v_mfma_i32_16x16x64_i8 v[70:73], v[146:149], v[174:177], v[70:73]
	s_nop 0
	v_mfma_i32_16x16x64_i8 v[70:73], v[138:141], v[170:173], v[70:73]
	v_mfma_i32_16x16x64_i8 v[78:81], v[134:137], v[174:177], v[78:81]
	s_nop 0
	v_mfma_i32_16x16x64_i8 v[78:81], v[130:133], v[170:173], v[78:81]
	v_mfma_i32_16x16x64_i8 v[90:93], v[158:161], v[166:169], v[90:93]
	s_nop 0
	v_mfma_i32_16x16x64_i8 v[90:93], v[154:157], v[162:165], v[90:93]
	v_mfma_i32_16x16x64_i8 v[106:109], v[150:153], v[166:169], v[106:109]
	s_nop 0
	v_mfma_i32_16x16x64_i8 v[106:109], v[142:145], v[162:165], v[106:109]
	v_mfma_i32_16x16x64_i8 v[102:105], v[146:149], v[166:169], v[102:105]
	s_nop 0
	v_mfma_i32_16x16x64_i8 v[102:105], v[138:141], v[162:165], v[102:105]
	v_mfma_i32_16x16x64_i8 v[110:113], v[134:137], v[166:169], v[110:113]
	s_nop 0
	v_mfma_i32_16x16x64_i8 v[110:113], v[130:133], v[162:165], v[110:113]
	s_setprio 0
	s_barrier
	s_add_u32 s43, s43, 0x100
	s_addc_u32 s74, s80, 0
	s_and_b64 s[64:65], s[66:67], exec
	s_cselect_b32 s65, s51, s74
	s_cselect_b32 s64, s50, s43
	s_add_u32 s50, s52, 0x80
	s_addc_u32 s51, s53, 0
	s_add_i32 s43, 0, 0x18000
	s_add_i32 s74, 0, 0x1c000
	v_add_u32_e32 v130, s43, v199
	v_add_u32_e32 v131, s74, v199
	ds_read_b128 v[158:161], v130
	ds_read_b128 v[154:157], v130 offset:1024
	ds_read_b128 v[150:153], v130 offset:2048
	ds_read_b128 v[146:149], v130 offset:3072
	ds_read_b128 v[142:145], v131
	ds_read_b128 v[138:141], v131 offset:1024
	ds_read_b128 v[134:137], v131 offset:2048
	ds_read_b128 v[130:133], v131 offset:3072
	s_mov_b64 s[66:67], s[64:65]
	v_mov_b32_e32 v203, v196
	s_mov_b32 m0, s5
	s_waitcnt lgkmcnt(0)
	ds_read_b128 v[162:165], v202 offset:32768
	ds_read_b128 v[166:169], v202 offset:33792
	ds_read_b128 v[170:173], v202 offset:34816
	ds_read_b128 v[174:177], v202 offset:35840
	ds_read_b128 v[178:181], v202 offset:36864
	ds_read_b128 v[182:185], v202 offset:37888
	ds_read_b128 v[186:189], v202 offset:38912
	ds_read_b128 v[190:193], v202 offset:39936
	s_add_u32 s64, s64, 0x40000
	global_load_lds_dwordx4 v203, s[66:67]
	v_mov_b32_e32 v203, v197
	s_mov_b32 m0, s62
	s_addc_u32 s65, s65, 0
	global_load_lds_dwordx4 v203, s[66:67]
	v_mov_b32_e32 v203, v196
	s_mov_b32 m0, s63
	s_nop 0
	global_load_lds_dwordx4 v203, s[64:65]
	v_mov_b32_e32 v203, v197
	s_mov_b32 m0, s69
	s_nop 0
	global_load_lds_dwordx4 v203, s[64:65]
	s_waitcnt vmcnt(8)
	s_waitcnt lgkmcnt(0)
	s_barrier
	s_setprio 1
	s_waitcnt lgkmcnt(0)
	v_mfma_i32_16x16x64_i8 v[18:21], v[158:161], v[162:165], v[18:21]
	s_nop 0
	v_mfma_i32_16x16x64_i8 v[18:21], v[154:157], v[166:169], v[18:21]
	v_mfma_i32_16x16x64_i8 v[22:25], v[150:153], v[162:165], v[22:25]
	s_nop 0
	v_mfma_i32_16x16x64_i8 v[22:25], v[146:149], v[166:169], v[22:25]
	v_mfma_i32_16x16x64_i8 v[26:29], v[142:145], v[162:165], v[26:29]
	s_nop 0
	v_mfma_i32_16x16x64_i8 v[26:29], v[138:141], v[166:169], v[26:29]
	v_mfma_i32_16x16x64_i8 v[34:37], v[134:137], v[162:165], v[34:37]
	s_nop 0
	v_mfma_i32_16x16x64_i8 v[34:37], v[130:133], v[166:169], v[34:37]
	v_mfma_i32_16x16x64_i8 v[50:53], v[158:161], v[170:173], v[50:53]
	s_nop 0
	v_mfma_i32_16x16x64_i8 v[50:53], v[154:157], v[174:177], v[50:53]
	v_mfma_i32_16x16x64_i8 v[62:65], v[150:153], v[170:173], v[62:65]
	s_nop 0
	v_mfma_i32_16x16x64_i8 v[62:65], v[146:149], v[174:177], v[62:65]
	v_mfma_i32_16x16x64_i8 v[54:57], v[142:145], v[170:173], v[54:57]
	s_nop 0
	v_mfma_i32_16x16x64_i8 v[54:57], v[138:141], v[174:177], v[54:57]
	v_mfma_i32_16x16x64_i8 v[66:69], v[134:137], v[170:173], v[66:69]
	s_nop 0
	v_mfma_i32_16x16x64_i8 v[66:69], v[130:133], v[174:177], v[66:69]
	v_mfma_i32_16x16x64_i8 v[82:85], v[158:161], v[178:181], v[82:85]
	s_nop 0
	v_mfma_i32_16x16x64_i8 v[82:85], v[154:157], v[182:185], v[82:85]
	v_mfma_i32_16x16x64_i8 v[94:97], v[150:153], v[178:181], v[94:97]
	s_nop 0
	v_mfma_i32_16x16x64_i8 v[94:97], v[146:149], v[182:185], v[94:97]
	v_mfma_i32_16x16x64_i8 v[86:89], v[142:145], v[178:181], v[86:89]
	s_nop 0
	v_mfma_i32_16x16x64_i8 v[86:89], v[138:141], v[182:185], v[86:89]
	v_mfma_i32_16x16x64_i8 v[98:101], v[134:137], v[178:181], v[98:101]
	s_nop 0
	v_mfma_i32_16x16x64_i8 v[98:101], v[130:133], v[182:185], v[98:101]
	v_mfma_i32_16x16x64_i8 v[114:117], v[158:161], v[186:189], v[114:117]
	s_nop 0
	v_mfma_i32_16x16x64_i8 v[114:117], v[154:157], v[190:193], v[114:117]
	v_mfma_i32_16x16x64_i8 v[122:125], v[150:153], v[186:189], v[122:125]
	s_nop 0
	v_mfma_i32_16x16x64_i8 v[122:125], v[146:149], v[190:193], v[122:125]
	v_mfma_i32_16x16x64_i8 v[118:121], v[142:145], v[186:189], v[118:121]
	s_nop 0
	v_mfma_i32_16x16x64_i8 v[118:121], v[138:141], v[190:193], v[118:121]
	v_mfma_i32_16x16x64_i8 v[126:129], v[134:137], v[186:189], v[126:129]
	s_nop 0
	v_mfma_i32_16x16x64_i8 v[126:129], v[130:133], v[190:193], v[126:129]
	s_setprio 0
	s_barrier
	v_mov_b32_e32 v203, v196
	s_add_i32 s43, s43, s10
	ds_read_b128 v[162:165], v202 offset:49152
	ds_read_b128 v[166:169], v202 offset:50176
	ds_read_b128 v[170:173], v202 offset:51200
	ds_read_b128 v[174:177], v202 offset:52224
	ds_read_b128 v[178:181], v202 offset:53248
	ds_read_b128 v[182:185], v202 offset:54272
	ds_read_b128 v[186:189], v202 offset:55296
	ds_read_b128 v[190:193], v202 offset:56320
	s_mov_b32 m0, s43
	s_nop 0
	global_load_lds_dwordx4 v203, s[50:51]
	v_mov_b32_e32 v203, v197
	s_add_i32 m0, s43, 0x2000
	s_nop 0
	global_load_lds_dwordx4 v203, s[50:51]
	s_add_u32 s50, s52, 0x40080
	s_addc_u32 s51, s53, 0
	v_mov_b32_e32 v203, v196
	s_add_i32 s43, s74, s10
	s_mov_b32 m0, s43
	s_nop 0
	global_load_lds_dwordx4 v203, s[50:51]
	v_mov_b32_e32 v203, v197
	s_add_i32 m0, s43, 0x2000
	s_nop 0
	global_load_lds_dwordx4 v203, s[50:51]
	s_waitcnt vmcnt(6)
	s_waitcnt lgkmcnt(0)
	s_barrier
	s_setprio 1
	s_waitcnt lgkmcnt(0)
	v_mfma_i32_16x16x64_i8 v[2:5], v[158:161], v[162:165], v[2:5]
	s_nop 0
	v_mfma_i32_16x16x64_i8 v[2:5], v[154:157], v[166:169], v[2:5]
	v_mfma_i32_16x16x64_i8 v[6:9], v[150:153], v[162:165], v[6:9]
	s_nop 0
	v_mfma_i32_16x16x64_i8 v[6:9], v[146:149], v[166:169], v[6:9]
	v_mfma_i32_16x16x64_i8 v[10:13], v[142:145], v[162:165], v[10:13]
	s_nop 0
	v_mfma_i32_16x16x64_i8 v[10:13], v[138:141], v[166:169], v[10:13]
	v_mfma_i32_16x16x64_i8 v[14:17], v[134:137], v[162:165], v[14:17]
	s_nop 0
	v_mfma_i32_16x16x64_i8 v[14:17], v[130:133], v[166:169], v[14:17]
	v_mfma_i32_16x16x64_i8 v[30:33], v[158:161], v[170:173], v[30:33]
	s_nop 0
	v_mfma_i32_16x16x64_i8 v[30:33], v[154:157], v[174:177], v[30:33]
	v_mfma_i32_16x16x64_i8 v[42:45], v[150:153], v[170:173], v[42:45]
	s_nop 0
	v_mfma_i32_16x16x64_i8 v[42:45], v[146:149], v[174:177], v[42:45]
	v_mfma_i32_16x16x64_i8 v[38:41], v[142:145], v[170:173], v[38:41]
	s_nop 0
	v_mfma_i32_16x16x64_i8 v[38:41], v[138:141], v[174:177], v[38:41]
	v_mfma_i32_16x16x64_i8 v[46:49], v[134:137], v[170:173], v[46:49]
	s_nop 0
	v_mfma_i32_16x16x64_i8 v[46:49], v[130:133], v[174:177], v[46:49]
	v_mfma_i32_16x16x64_i8 v[58:61], v[158:161], v[178:181], v[58:61]
	s_nop 0
	v_mfma_i32_16x16x64_i8 v[58:61], v[154:157], v[182:185], v[58:61]
	v_mfma_i32_16x16x64_i8 v[74:77], v[150:153], v[178:181], v[74:77]
	s_nop 0
	v_mfma_i32_16x16x64_i8 v[74:77], v[146:149], v[182:185], v[74:77]
	v_mfma_i32_16x16x64_i8 v[70:73], v[142:145], v[178:181], v[70:73]
	s_nop 0
	v_mfma_i32_16x16x64_i8 v[70:73], v[138:141], v[182:185], v[70:73]
	v_mfma_i32_16x16x64_i8 v[78:81], v[134:137], v[178:181], v[78:81]
	s_nop 0
	v_mfma_i32_16x16x64_i8 v[78:81], v[130:133], v[182:185], v[78:81]
	v_mfma_i32_16x16x64_i8 v[90:93], v[158:161], v[186:189], v[90:93]
	s_nop 0
	v_mfma_i32_16x16x64_i8 v[90:93], v[154:157], v[190:193], v[90:93]
	v_mfma_i32_16x16x64_i8 v[106:109], v[150:153], v[186:189], v[106:109]
	s_nop 0
	v_mfma_i32_16x16x64_i8 v[106:109], v[146:149], v[190:193], v[106:109]
	v_mfma_i32_16x16x64_i8 v[102:105], v[142:145], v[186:189], v[102:105]
	s_nop 0
	v_mfma_i32_16x16x64_i8 v[102:105], v[138:141], v[190:193], v[102:105]
	v_mfma_i32_16x16x64_i8 v[110:113], v[134:137], v[186:189], v[110:113]
	s_nop 0
	v_mfma_i32_16x16x64_i8 v[110:113], v[130:133], v[190:193], v[110:113]
	s_setprio 0
	s_barrier
	s_add_i32 s41, s41, 2
	s_add_u32 s48, s48, 0x100
	s_addc_u32 s49, s49, 0
	s_cmp_gt_u32 s41, 13
	s_cbranch_scc1 .LBB0_1308
	s_mov_b64 s[52:53], s[14:15]
	s_mov_b64 s[50:51], s[18:19]
	s_branch .Li8loop_1294
